# fp8 GEMM K-loops (P1,P7,P10,P11,P14): the six-piece load segments hand their A half-tile stage (2 LDS-DMA pieces) to the following MFMA segment; that phase's counted wait vmcnt(8)->vmcnt(6)
# speedup vs baseline: 1.0058x; 1.0058x over previous
; #define PG8_STAGE(bufoff, gbase, voff) do { _Pragma("unroll") for (int _i = 0; _i < 2; ++_i) \
;         asm volatile("s_mov_b32 m0, %0\n\ts_nop 0\n\tglobal_load_lds_dwordx4 %1, %2" :: "s"(ldsb + (unsigned)(bufoff) + ldsw + _i * 8192u), "v"((voff)[_i]), "s"((const char*)(gbase)) : "m0", "memory"); } while (0)
; #define PG8_WAIT_V(n) asm volatile("s_waitcnt vmcnt(" #n ")" ::: "memory")
; #define PG8_WAIT_L(n) asm volatile("s_waitcnt lgkmcnt(" #n ")" ::: "memory")
; #define PG8_BAR __builtin_amdgcn_s_barrier()
; #define PG8_SCHED __builtin_amdgcn_sched_barrier(0)
; template <class Epi, class Sched, bool F8 = false, bool MID = false, bool GATHER = false>
; __device__ __forceinline__ void gemm_phase(LAS unsigned char* lds, const Gemm g, const Sched& S, const Epi& E) {
;     ...
;             PG8_LDB(B0, 0, 0); PG8_LDB(B1, 0, 1); PG8_SCHED; PG8_LDA(At, 0, 0); PG8_STAGE(PG8_SA(1, 1), a1, voffA1);
;             PG8_WAIT_V(8); PG8_WAIT_L(0); PG8_BAR; PG8_MMA(0, 0, At, B0); PG8_MMA(0, 1, At, B1); PG8_BAR; PG8_SCHED;
;             PG8_LDA(At, 0, 1); PG8_STAGE(PG8_SB(0, 0), b2, voffB); PG8_STAGE(PG8_SB(0, 1), b2 + hstepB, voffB); PG8_STAGE(PG8_SA(0, 0), a2, xA0);
;             PG8_WAIT_V(8); PG8_WAIT_L(0); PG8_BAR; PG8_MMA(1, 0, At, B0); PG8_MMA(1, 1, At, B1); PG8_BAR; PG8_SCHED;
.LBB0_1161:
	ds_read_b128 v[18:21], v170
	ds_read_b128 v[22:25], v170 offset:1024
	ds_read_b128 v[26:29], v170 offset:2048
	ds_read_b128 v[30:33], v170 offset:3072
	s_waitcnt lgkmcnt(4)
	ds_read_b128 v[2:5], v171
	ds_read_b128 v[6:9], v171 offset:1024
	ds_read_b128 v[10:13], v171 offset:2048
	ds_read_b128 v[14:17], v171 offset:3072
	s_add_u32 s4, s54, 0x100
	s_addc_u32 s5, s55, 0
	s_cmp_eq_u32 s79, 12
	s_cselect_b32 s60, s48, s4
	s_cselect_b32 s61, s49, s5
	s_cselect_b32 s56, s50, vcc_lo
	s_cselect_b32 s57, s51, vcc_hi
	s_add_u32 s58, s60, 0x80
	s_addc_u32 s59, s61, 0
	s_add_u32 s54, s54, 0x80
	s_addc_u32 s55, s55, 0
	ds_read_b128 v[178:181], v172
	ds_read_b128 v[182:185], v172 offset:1024
	ds_read_b128 v[186:189], v172 offset:2048
	ds_read_b128 v[190:193], v172 offset:3072
	ds_read_b128 v[194:197], v172 offset:4096
	ds_read_b128 v[198:201], v172 offset:5120
	ds_read_b128 v[202:205], v172 offset:6144
	ds_read_b128 v[206:209], v172 offset:7168
	s_mov_b32 m0, s89
	s_nop 0
	global_load_lds_dwordx4 v163, s[54:55]
	s_nop 0
	s_mov_b32 m0, s90
	s_nop 0
	global_load_lds_dwordx4 v168, s[54:55]
	s_waitcnt vmcnt(8)
	s_waitcnt lgkmcnt(0)
	s_barrier
	s_setprio 1
	s_waitcnt lgkmcnt(6)
	v_mfma_scale_f32_16x16x128_f8f6f4 v[158:161], v[18:25], v[178:185], v[158:161], v173, v174 op_sel_hi:[0,0,0]
	v_mfma_scale_f32_16x16x128_f8f6f4 v[154:157], v[26:33], v[178:185], v[154:157], v173, v174 op_sel_hi:[0,0,0]
	s_waitcnt lgkmcnt(4)
	v_mfma_scale_f32_16x16x128_f8f6f4 v[142:145], v[18:25], v[186:193], v[142:145], v173, v174 op_sel_hi:[0,0,0]
	v_mfma_scale_f32_16x16x128_f8f6f4 v[138:141], v[26:33], v[186:193], v[138:141], v173, v174 op_sel_hi:[0,0,0]
	s_waitcnt lgkmcnt(2)
	v_mfma_scale_f32_16x16x128_f8f6f4 v[130:133], v[18:25], v[194:201], v[130:133], v173, v174 op_sel_hi:[0,0,0]
	v_mfma_scale_f32_16x16x128_f8f6f4 v[122:125], v[26:33], v[194:201], v[122:125], v173, v174 op_sel_hi:[0,0,0]
	s_waitcnt lgkmcnt(0)
	v_mfma_scale_f32_16x16x128_f8f6f4 v[114:117], v[18:25], v[202:209], v[114:117], v173, v174 op_sel_hi:[0,0,0]
	v_mfma_scale_f32_16x16x128_f8f6f4 v[106:109], v[26:33], v[202:209], v[106:109], v173, v174 op_sel_hi:[0,0,0]
	s_setprio 0
	s_setprio 1
	v_mfma_scale_f32_16x16x128_f8f6f4 v[150:153], v[2:9], v[178:185], v[150:153], v173, v174 op_sel_hi:[0,0,0]
	v_mfma_scale_f32_16x16x128_f8f6f4 v[146:149], v[10:17], v[178:185], v[146:149], v173, v174 op_sel_hi:[0,0,0]
	v_mfma_scale_f32_16x16x128_f8f6f4 v[134:137], v[2:9], v[186:193], v[134:137], v173, v174 op_sel_hi:[0,0,0]
	v_mfma_scale_f32_16x16x128_f8f6f4 v[126:129], v[10:17], v[186:193], v[126:129], v173, v174 op_sel_hi:[0,0,0]
	v_mfma_scale_f32_16x16x128_f8f6f4 v[118:121], v[2:9], v[194:201], v[118:121], v173, v174 op_sel_hi:[0,0,0]
	v_mfma_scale_f32_16x16x128_f8f6f4 v[110:113], v[10:17], v[194:201], v[110:113], v173, v174 op_sel_hi:[0,0,0]
	v_mfma_scale_f32_16x16x128_f8f6f4 v[102:105], v[2:9], v[202:209], v[102:105], v173, v174 op_sel_hi:[0,0,0]
	v_mfma_scale_f32_16x16x128_f8f6f4 v[98:101], v[10:17], v[202:209], v[98:101], v173, v174 op_sel_hi:[0,0,0]
	s_setprio 0
	s_barrier
	ds_read_b128 v[178:181], v172 offset:16384
	ds_read_b128 v[182:185], v172 offset:17408
	ds_read_b128 v[186:189], v172 offset:18432
	ds_read_b128 v[190:193], v172 offset:19456
	ds_read_b128 v[194:197], v172 offset:20480
	ds_read_b128 v[198:201], v172 offset:21504
	ds_read_b128 v[202:205], v172 offset:22528
	ds_read_b128 v[206:209], v172 offset:23552
	s_mov_b32 m0, s26
	s_nop 0
	global_load_lds_dwordx4 v165, s[56:57]
	s_add_u32 s54, s56, 0x40000
	s_mov_b32 m0, s27
	s_nop 0
	global_load_lds_dwordx4 v169, s[56:57]
	s_addc_u32 s55, s57, 0
	s_mov_b32 m0, s62
	s_nop 0
	global_load_lds_dwordx4 v165, s[54:55]
	s_nop 0
	s_mov_b32 m0, s63
	s_nop 0
	global_load_lds_dwordx4 v169, s[54:55]
	s_nop 0
	s_waitcnt vmcnt(6)
	s_waitcnt lgkmcnt(0)
	s_barrier
	s_setprio 1
	s_waitcnt lgkmcnt(6)
	v_mfma_scale_f32_16x16x128_f8f6f4 v[94:97], v[18:25], v[178:185], v[94:97], v173, v174 op_sel_hi:[0,0,0]
	v_mfma_scale_f32_16x16x128_f8f6f4 v[90:93], v[26:33], v[178:185], v[90:93], v173, v174 op_sel_hi:[0,0,0]
	s_mov_b32 m0, s3
	s_nop 0
	global_load_lds_dwordx4 v162, s[60:61]
	s_waitcnt lgkmcnt(4)
	v_mfma_scale_f32_16x16x128_f8f6f4 v[70:73], v[18:25], v[186:193], v[70:73], v173, v174 op_sel_hi:[0,0,0]
	v_mfma_scale_f32_16x16x128_f8f6f4 v[66:69], v[26:33], v[186:193], v[66:69], v173, v174 op_sel_hi:[0,0,0]
	s_mov_b32 m0, s64
	s_nop 0
	global_load_lds_dwordx4 v167, s[60:61]
	s_waitcnt lgkmcnt(2)
	v_mfma_scale_f32_16x16x128_f8f6f4 v[50:53], v[18:25], v[194:201], v[50:53], v173, v174 op_sel_hi:[0,0,0]
	v_mfma_scale_f32_16x16x128_f8f6f4 v[42:45], v[26:33], v[194:201], v[42:45], v173, v174 op_sel_hi:[0,0,0]
	s_waitcnt lgkmcnt(0)
	v_mfma_scale_f32_16x16x128_f8f6f4 v[38:41], v[18:25], v[202:209], v[38:41], v173, v174 op_sel_hi:[0,0,0]
	v_mfma_scale_f32_16x16x128_f8f6f4 v[34:37], v[26:33], v[202:209], v[34:37], v173, v174 op_sel_hi:[0,0,0]
	s_setprio 0
	s_setprio 1
	v_mfma_scale_f32_16x16x128_f8f6f4 v[86:89], v[2:9], v[178:185], v[86:89], v173, v174 op_sel_hi:[0,0,0]
	v_mfma_scale_f32_16x16x128_f8f6f4 v[74:77], v[10:17], v[178:185], v[74:77], v173, v174 op_sel_hi:[0,0,0]
	v_mfma_scale_f32_16x16x128_f8f6f4 v[54:57], v[2:9], v[186:193], v[54:57], v173, v174 op_sel_hi:[0,0,0]
	v_mfma_scale_f32_16x16x128_f8f6f4 v[46:49], v[10:17], v[186:193], v[46:49], v173, v174 op_sel_hi:[0,0,0]
	v_mfma_scale_f32_16x16x128_f8f6f4 v[82:85], v[2:9], v[194:201], v[82:85], v173, v174 op_sel_hi:[0,0,0]
	v_mfma_scale_f32_16x16x128_f8f6f4 v[78:81], v[10:17], v[194:201], v[78:81], v173, v174 op_sel_hi:[0,0,0]
	v_mfma_scale_f32_16x16x128_f8f6f4 v[62:65], v[2:9], v[202:209], v[62:65], v173, v174 op_sel_hi:[0,0,0]
	v_mfma_scale_f32_16x16x128_f8f6f4 v[58:61], v[10:17], v[202:209], v[58:61], v173, v174 op_sel_hi:[0,0,0]
	s_setprio 0
	s_barrier
; #define PG8_STAGE(bufoff, gbase, voff) do { _Pragma("unroll") for (int _i = 0; _i < 2; ++_i) \
;         asm volatile("s_mov_b32 m0, %0\n\ts_nop 0\n\tglobal_load_lds_dwordx4 %1, %2" :: "s"(ldsb + (unsigned)(bufoff) + ldsw + _i * 8192u), "v"((voff)[_i]), "s"((const char*)(gbase)) : "m0", "memory"); } while (0)
; #define PG8_WAIT_V(n) asm volatile("s_waitcnt vmcnt(" #n ")" ::: "memory")
; #define PG8_WAIT_L(n) asm volatile("s_waitcnt lgkmcnt(" #n ")" ::: "memory")
; #define PG8_BAR __builtin_amdgcn_s_barrier()
; #define PG8_SCHED __builtin_amdgcn_sched_barrier(0)
; template <class Epi, class Sched, bool F8 = false, bool MID = false, bool GATHER = false>
; __device__ __forceinline__ void gemm_phase(LAS unsigned char* lds, const Gemm g, const Sched& S, const Epi& E) {
;     ...
;             PG8_LDB(B0, 1, 0); PG8_LDB(B1, 1, 1); PG8_SCHED; PG8_LDA(At, 1, 0); PG8_STAGE(PG8_SA(0, 1), a2, xA1);
;             PG8_WAIT_V(8); PG8_WAIT_L(0); PG8_BAR; PG8_MMA(0, 0, At, B0); PG8_MMA(0, 1, At, B1); PG8_BAR; PG8_SCHED;
;             PG8_LDA(At, 1, 1); PG8_STAGE(PG8_SB(1, 0), b3, voffB); PG8_STAGE(PG8_SB(1, 1), b3 + hstepB, voffB); PG8_STAGE(PG8_SA(1, 0), a3, xA0);
;             PG8_WAIT_V(8); PG8_WAIT_L(0); PG8_BAR; PG8_MMA(1, 0, At, B0); PG8_MMA(1, 1, At, B1); PG8_BAR; PG8_SCHED;
	ds_read_b128 v[2:5], v175
	ds_read_b128 v[6:9], v175 offset:1024
	ds_read_b128 v[10:13], v175 offset:2048
	ds_read_b128 v[14:17], v175 offset:3072
	ds_read_b128 v[18:21], v176
	ds_read_b128 v[22:25], v176 offset:1024
	ds_read_b128 v[26:29], v176 offset:2048
	ds_read_b128 v[30:33], v176 offset:3072
	ds_read_b128 v[178:181], v172 offset:32768
	ds_read_b128 v[182:185], v172 offset:33792
	ds_read_b128 v[186:189], v172 offset:34816
	ds_read_b128 v[190:193], v172 offset:35840
	ds_read_b128 v[194:197], v172 offset:36864
	ds_read_b128 v[198:201], v172 offset:37888
	ds_read_b128 v[202:205], v172 offset:38912
	ds_read_b128 v[206:209], v172 offset:39936
	s_mov_b32 m0, s65
	s_nop 0
	global_load_lds_dwordx4 v163, s[60:61]
	s_nop 0
	s_mov_b32 m0, s66
	s_nop 0
	global_load_lds_dwordx4 v168, s[60:61]
	s_waitcnt vmcnt(8)
	s_waitcnt lgkmcnt(0)
	s_barrier
	s_setprio 1
	s_waitcnt lgkmcnt(6)
	v_mfma_scale_f32_16x16x128_f8f6f4 v[158:161], v[2:9], v[178:185], v[158:161], v173, v174 op_sel_hi:[0,0,0]
	v_mfma_scale_f32_16x16x128_f8f6f4 v[154:157], v[10:17], v[178:185], v[154:157], v173, v174 op_sel_hi:[0,0,0]
	s_waitcnt lgkmcnt(4)
	v_mfma_scale_f32_16x16x128_f8f6f4 v[142:145], v[2:9], v[186:193], v[142:145], v173, v174 op_sel_hi:[0,0,0]
	v_mfma_scale_f32_16x16x128_f8f6f4 v[138:141], v[10:17], v[186:193], v[138:141], v173, v174 op_sel_hi:[0,0,0]
	s_waitcnt lgkmcnt(2)
	v_mfma_scale_f32_16x16x128_f8f6f4 v[130:133], v[2:9], v[194:201], v[130:133], v173, v174 op_sel_hi:[0,0,0]
	v_mfma_scale_f32_16x16x128_f8f6f4 v[122:125], v[10:17], v[194:201], v[122:125], v173, v174 op_sel_hi:[0,0,0]
	s_waitcnt lgkmcnt(0)
	v_mfma_scale_f32_16x16x128_f8f6f4 v[114:117], v[2:9], v[202:209], v[114:117], v173, v174 op_sel_hi:[0,0,0]
	v_mfma_scale_f32_16x16x128_f8f6f4 v[106:109], v[10:17], v[202:209], v[106:109], v173, v174 op_sel_hi:[0,0,0]
	s_setprio 0
	s_setprio 1
	v_mfma_scale_f32_16x16x128_f8f6f4 v[150:153], v[18:25], v[178:185], v[150:153], v173, v174 op_sel_hi:[0,0,0]
	v_mfma_scale_f32_16x16x128_f8f6f4 v[146:149], v[26:33], v[178:185], v[146:149], v173, v174 op_sel_hi:[0,0,0]
	v_mfma_scale_f32_16x16x128_f8f6f4 v[134:137], v[18:25], v[186:193], v[134:137], v173, v174 op_sel_hi:[0,0,0]
	v_mfma_scale_f32_16x16x128_f8f6f4 v[126:129], v[26:33], v[186:193], v[126:129], v173, v174 op_sel_hi:[0,0,0]
	v_mfma_scale_f32_16x16x128_f8f6f4 v[118:121], v[18:25], v[194:201], v[118:121], v173, v174 op_sel_hi:[0,0,0]
	v_mfma_scale_f32_16x16x128_f8f6f4 v[110:113], v[26:33], v[194:201], v[110:113], v173, v174 op_sel_hi:[0,0,0]
	v_mfma_scale_f32_16x16x128_f8f6f4 v[102:105], v[18:25], v[202:209], v[102:105], v173, v174 op_sel_hi:[0,0,0]
	v_mfma_scale_f32_16x16x128_f8f6f4 v[98:101], v[26:33], v[202:209], v[98:101], v173, v174 op_sel_hi:[0,0,0]
	s_setprio 0
	s_barrier
	ds_read_b128 v[178:181], v172 offset:49152
	ds_read_b128 v[182:185], v172 offset:50176
	ds_read_b128 v[186:189], v172 offset:51200
	ds_read_b128 v[190:193], v172 offset:52224
	ds_read_b128 v[194:197], v172 offset:53248
	ds_read_b128 v[198:201], v172 offset:54272
	ds_read_b128 v[202:205], v172 offset:55296
	ds_read_b128 v[206:209], v172 offset:56320
	s_add_u32 s54, s56, 0x80
	s_addc_u32 s55, s57, 0
	s_mov_b32 m0, s70
	s_nop 0
	global_load_lds_dwordx4 v165, s[54:55]
	s_nop 0
	s_mov_b32 m0, s71
	s_nop 0
	global_load_lds_dwordx4 v169, s[54:55]
	s_add_u32 s54, s56, 0x40080
	s_addc_u32 s55, s57, 0
	s_mov_b32 m0, s87
	s_nop 0
	global_load_lds_dwordx4 v165, s[54:55]
	s_nop 0
	s_mov_b32 m0, s88
	s_nop 0
	global_load_lds_dwordx4 v169, s[54:55]
	s_nop 0
	s_waitcnt vmcnt(6)
	s_waitcnt lgkmcnt(0)
	s_barrier
	s_setprio 1
	s_waitcnt lgkmcnt(6)
	v_mfma_scale_f32_16x16x128_f8f6f4 v[94:97], v[2:9], v[178:185], v[94:97], v173, v174 op_sel_hi:[0,0,0]
	v_mfma_scale_f32_16x16x128_f8f6f4 v[90:93], v[10:17], v[178:185], v[90:93], v173, v174 op_sel_hi:[0,0,0]
	s_mov_b32 m0, s72
	s_nop 0
	global_load_lds_dwordx4 v162, s[58:59]
	s_waitcnt lgkmcnt(4)
	v_mfma_scale_f32_16x16x128_f8f6f4 v[70:73], v[2:9], v[186:193], v[70:73], v173, v174 op_sel_hi:[0,0,0]
	v_mfma_scale_f32_16x16x128_f8f6f4 v[66:69], v[10:17], v[186:193], v[66:69], v173, v174 op_sel_hi:[0,0,0]
	s_mov_b32 m0, s73
	s_nop 0
	global_load_lds_dwordx4 v167, s[58:59]
	s_waitcnt lgkmcnt(2)
	v_mfma_scale_f32_16x16x128_f8f6f4 v[50:53], v[2:9], v[194:201], v[50:53], v173, v174 op_sel_hi:[0,0,0]
	v_mfma_scale_f32_16x16x128_f8f6f4 v[42:45], v[10:17], v[194:201], v[42:45], v173, v174 op_sel_hi:[0,0,0]
	s_waitcnt lgkmcnt(0)
	v_mfma_scale_f32_16x16x128_f8f6f4 v[38:41], v[2:9], v[202:209], v[38:41], v173, v174 op_sel_hi:[0,0,0]
	v_mfma_scale_f32_16x16x128_f8f6f4 v[34:37], v[10:17], v[202:209], v[34:37], v173, v174 op_sel_hi:[0,0,0]
	s_setprio 0
	s_setprio 1
	v_mfma_scale_f32_16x16x128_f8f6f4 v[86:89], v[18:25], v[178:185], v[86:89], v173, v174 op_sel_hi:[0,0,0]
	v_mfma_scale_f32_16x16x128_f8f6f4 v[74:77], v[26:33], v[178:185], v[74:77], v173, v174 op_sel_hi:[0,0,0]
	v_mfma_scale_f32_16x16x128_f8f6f4 v[54:57], v[18:25], v[186:193], v[54:57], v173, v174 op_sel_hi:[0,0,0]
	v_mfma_scale_f32_16x16x128_f8f6f4 v[46:49], v[26:33], v[186:193], v[46:49], v173, v174 op_sel_hi:[0,0,0]
	v_mfma_scale_f32_16x16x128_f8f6f4 v[82:85], v[18:25], v[194:201], v[82:85], v173, v174 op_sel_hi:[0,0,0]
	v_mfma_scale_f32_16x16x128_f8f6f4 v[78:81], v[26:33], v[194:201], v[78:81], v173, v174 op_sel_hi:[0,0,0]
	v_mfma_scale_f32_16x16x128_f8f6f4 v[62:65], v[18:25], v[202:209], v[62:65], v173, v174 op_sel_hi:[0,0,0]
	v_mfma_scale_f32_16x16x128_f8f6f4 v[58:61], v[26:33], v[202:209], v[58:61], v173, v174 op_sel_hi:[0,0,0]
	s_setprio 0
	s_barrier
	s_add_i32 s79, s79, 2
	s_add_u32 vcc_lo, vcc_lo, 0x100
	s_addc_u32 vcc_hi, vcc_hi, 0
	s_cmp_gt_u32 s79, 13
	s_mov_b64 s[54:55], s[4:5]
	s_cbranch_scc0 .LBB0_1161
	s_and_b64 vcc, exec, s[42:43]
	s_cbranch_vccz .LBB0_1164
	s_barrier

; #define PG8_STAGE(bufoff, gbase, voff) do { _Pragma("unroll") for (int _i = 0; _i < 2; ++_i) \
;         asm volatile("s_mov_b32 m0, %0\n\ts_nop 0\n\tglobal_load_lds_dwordx4 %1, %2" :: "s"(ldsb + (unsigned)(bufoff) + ldsw + _i * 8192u), "v"((voff)[_i]), "s"((const char*)(gbase)) : "m0", "memory"); } while (0)
; #define PG8_WAIT_V(n) asm volatile("s_waitcnt vmcnt(" #n ")" ::: "memory")
; #define PG8_WAIT_L(n) asm volatile("s_waitcnt lgkmcnt(" #n ")" ::: "memory")
; #define PG8_BAR __builtin_amdgcn_s_barrier()
; #define PG8_SCHED __builtin_amdgcn_sched_barrier(0)
; template <class Epi, class Sched, bool F8 = false, bool MID = false, bool GATHER = false>
; __device__ __forceinline__ void gemm_phase(LAS unsigned char* lds, const Gemm g, const Sched& S, const Epi& E) {
;     ...
;             PG8_LDB(B0, 0, 0); PG8_LDB(B1, 0, 1); PG8_SCHED; PG8_LDA(At, 0, 0); PG8_STAGE(PG8_SA(1, 1), a1, voffA1);
;             PG8_WAIT_V(8); PG8_WAIT_L(0); PG8_BAR; PG8_MMA(0, 0, At, B0); PG8_MMA(0, 1, At, B1); PG8_BAR; PG8_SCHED;
;             PG8_LDA(At, 0, 1); PG8_STAGE(PG8_SB(0, 0), b2, voffB); PG8_STAGE(PG8_SB(0, 1), b2 + hstepB, voffB); PG8_STAGE(PG8_SA(0, 0), a2, xA0);
;             PG8_WAIT_V(8); PG8_WAIT_L(0); PG8_BAR; PG8_MMA(1, 0, At, B0); PG8_MMA(1, 1, At, B1); PG8_BAR; PG8_SCHED;
.LBB0_1931:
	ds_read_b128 v[18:21], v169
	ds_read_b128 v[22:25], v169 offset:1024
	ds_read_b128 v[26:29], v169 offset:2048
	ds_read_b128 v[30:33], v169 offset:3072
	ds_read_b128 v[2:5], v170
	ds_read_b128 v[6:9], v170 offset:1024
	ds_read_b128 v[10:13], v170 offset:2048
	ds_read_b128 v[14:17], v170 offset:3072
	s_add_u32 s52, s54, 0x100
	s_addc_u32 s53, s55, 0
	s_cmp_eq_u32 s96, 12
	s_cselect_b32 s60, s48, s52
	s_cselect_b32 s61, s49, s53
	s_cselect_b32 s56, s50, s94
	s_cselect_b32 s57, s51, s95
	s_add_u32 s58, s60, 0x80
	s_addc_u32 s59, s61, 0
	s_add_u32 s54, s54, 0x80
	s_addc_u32 s55, s55, 0
	ds_read_b128 v[176:179], v171
	ds_read_b128 v[180:183], v171 offset:1024
	ds_read_b128 v[184:187], v171 offset:2048
	ds_read_b128 v[188:191], v171 offset:3072
	ds_read_b128 v[192:195], v171 offset:4096
	ds_read_b128 v[196:199], v171 offset:5120
	ds_read_b128 v[200:203], v171 offset:6144
	ds_read_b128 v[204:207], v171 offset:7168
	s_mov_b32 m0, s77
	s_nop 0
	global_load_lds_dwordx4 v162, s[54:55]
	s_nop 0
	s_mov_b32 m0, s78
	s_nop 0
	global_load_lds_dwordx4 v167, s[54:55]
	s_waitcnt vmcnt(8)
	s_waitcnt lgkmcnt(0)
	s_barrier
	s_setprio 1
	s_waitcnt lgkmcnt(6)
	v_mfma_scale_f32_16x16x128_f8f6f4 v[158:161], v[18:25], v[176:183], v[158:161], v172, v173 op_sel_hi:[0,0,0]
	v_mfma_scale_f32_16x16x128_f8f6f4 v[154:157], v[26:33], v[176:183], v[154:157], v172, v173 op_sel_hi:[0,0,0]
	s_waitcnt lgkmcnt(4)
	v_mfma_scale_f32_16x16x128_f8f6f4 v[150:153], v[18:25], v[184:191], v[150:153], v172, v173 op_sel_hi:[0,0,0]
	v_mfma_scale_f32_16x16x128_f8f6f4 v[142:145], v[26:33], v[184:191], v[142:145], v172, v173 op_sel_hi:[0,0,0]
	s_waitcnt lgkmcnt(2)
	v_mfma_scale_f32_16x16x128_f8f6f4 v[134:137], v[18:25], v[192:199], v[134:137], v172, v173 op_sel_hi:[0,0,0]
	v_mfma_scale_f32_16x16x128_f8f6f4 v[126:129], v[26:33], v[192:199], v[126:129], v172, v173 op_sel_hi:[0,0,0]
	s_waitcnt lgkmcnt(0)
	v_mfma_scale_f32_16x16x128_f8f6f4 v[118:121], v[18:25], v[200:207], v[118:121], v172, v173 op_sel_hi:[0,0,0]
	v_mfma_scale_f32_16x16x128_f8f6f4 v[110:113], v[26:33], v[200:207], v[110:113], v172, v173 op_sel_hi:[0,0,0]
	s_setprio 0
	s_setprio 1
	v_mfma_scale_f32_16x16x128_f8f6f4 v[146:149], v[2:9], v[176:183], v[146:149], v172, v173 op_sel_hi:[0,0,0]
	v_mfma_scale_f32_16x16x128_f8f6f4 v[138:141], v[10:17], v[176:183], v[138:141], v172, v173 op_sel_hi:[0,0,0]
	v_mfma_scale_f32_16x16x128_f8f6f4 v[130:133], v[2:9], v[184:191], v[130:133], v172, v173 op_sel_hi:[0,0,0]
	v_mfma_scale_f32_16x16x128_f8f6f4 v[122:125], v[10:17], v[184:191], v[122:125], v172, v173 op_sel_hi:[0,0,0]
	v_mfma_scale_f32_16x16x128_f8f6f4 v[114:117], v[2:9], v[192:199], v[114:117], v172, v173 op_sel_hi:[0,0,0]
	v_mfma_scale_f32_16x16x128_f8f6f4 v[106:109], v[10:17], v[192:199], v[106:109], v172, v173 op_sel_hi:[0,0,0]
	v_mfma_scale_f32_16x16x128_f8f6f4 v[102:105], v[2:9], v[200:207], v[102:105], v172, v173 op_sel_hi:[0,0,0]
	v_mfma_scale_f32_16x16x128_f8f6f4 v[98:101], v[10:17], v[200:207], v[98:101], v172, v173 op_sel_hi:[0,0,0]
	s_setprio 0
	s_barrier
	ds_read_b128 v[176:179], v171 offset:16384
	ds_read_b128 v[180:183], v171 offset:17408
	ds_read_b128 v[184:187], v171 offset:18432
	ds_read_b128 v[188:191], v171 offset:19456
	ds_read_b128 v[192:195], v171 offset:20480
	ds_read_b128 v[196:199], v171 offset:21504
	ds_read_b128 v[200:203], v171 offset:22528
	ds_read_b128 v[204:207], v171 offset:23552
	s_mov_b32 m0, s27
	s_nop 0
	global_load_lds_dwordx4 v163, s[56:57]
	s_add_u32 s54, s56, 0x40000
	s_mov_b32 m0, s62
	s_nop 0
	global_load_lds_dwordx4 v168, s[56:57]
	s_addc_u32 s55, s57, 0
	s_mov_b32 m0, s63
	s_nop 0
	global_load_lds_dwordx4 v163, s[54:55]
	s_nop 0
	s_mov_b32 m0, s64
	s_nop 0
	global_load_lds_dwordx4 v168, s[54:55]
	s_nop 0
	s_waitcnt vmcnt(6)
	s_waitcnt lgkmcnt(0)
	s_barrier
	s_setprio 1
	s_waitcnt lgkmcnt(6)
	v_mfma_scale_f32_16x16x128_f8f6f4 v[94:97], v[18:25], v[176:183], v[94:97], v172, v173 op_sel_hi:[0,0,0]
	v_mfma_scale_f32_16x16x128_f8f6f4 v[90:93], v[26:33], v[176:183], v[90:93], v172, v173 op_sel_hi:[0,0,0]
	s_mov_b32 m0, s26
	s_nop 0
	global_load_lds_dwordx4 v1, s[60:61]
	s_waitcnt lgkmcnt(4)
	v_mfma_scale_f32_16x16x128_f8f6f4 v[78:81], v[18:25], v[184:191], v[78:81], v172, v173 op_sel_hi:[0,0,0]
	v_mfma_scale_f32_16x16x128_f8f6f4 v[70:73], v[26:33], v[184:191], v[70:73], v172, v173 op_sel_hi:[0,0,0]
	s_mov_b32 m0, s65
	s_nop 0
	global_load_lds_dwordx4 v165, s[60:61]
	s_waitcnt lgkmcnt(2)
	v_mfma_scale_f32_16x16x128_f8f6f4 v[54:57], v[18:25], v[192:199], v[54:57], v172, v173 op_sel_hi:[0,0,0]
	v_mfma_scale_f32_16x16x128_f8f6f4 v[46:49], v[26:33], v[192:199], v[46:49], v172, v173 op_sel_hi:[0,0,0]
	s_waitcnt lgkmcnt(0)
	v_mfma_scale_f32_16x16x128_f8f6f4 v[38:41], v[18:25], v[200:207], v[38:41], v172, v173 op_sel_hi:[0,0,0]
	v_mfma_scale_f32_16x16x128_f8f6f4 v[34:37], v[26:33], v[200:207], v[34:37], v172, v173 op_sel_hi:[0,0,0]
	s_setprio 0
	s_setprio 1
	v_mfma_scale_f32_16x16x128_f8f6f4 v[74:77], v[2:9], v[176:183], v[74:77], v172, v173 op_sel_hi:[0,0,0]
	v_mfma_scale_f32_16x16x128_f8f6f4 v[62:65], v[10:17], v[176:183], v[62:65], v172, v173 op_sel_hi:[0,0,0]
	v_mfma_scale_f32_16x16x128_f8f6f4 v[50:53], v[2:9], v[184:191], v[50:53], v172, v173 op_sel_hi:[0,0,0]
	v_mfma_scale_f32_16x16x128_f8f6f4 v[42:45], v[10:17], v[184:191], v[42:45], v172, v173 op_sel_hi:[0,0,0]
	v_mfma_scale_f32_16x16x128_f8f6f4 v[86:89], v[2:9], v[192:199], v[86:89], v172, v173 op_sel_hi:[0,0,0]
	v_mfma_scale_f32_16x16x128_f8f6f4 v[82:85], v[10:17], v[192:199], v[82:85], v172, v173 op_sel_hi:[0,0,0]
	v_mfma_scale_f32_16x16x128_f8f6f4 v[66:69], v[2:9], v[200:207], v[66:69], v172, v173 op_sel_hi:[0,0,0]
	v_mfma_scale_f32_16x16x128_f8f6f4 v[58:61], v[10:17], v[200:207], v[58:61], v172, v173 op_sel_hi:[0,0,0]
	s_setprio 0
	s_barrier
; #define PG8_STAGE(bufoff, gbase, voff) do { _Pragma("unroll") for (int _i = 0; _i < 2; ++_i) \
;         asm volatile("s_mov_b32 m0, %0\n\ts_nop 0\n\tglobal_load_lds_dwordx4 %1, %2" :: "s"(ldsb + (unsigned)(bufoff) + ldsw + _i * 8192u), "v"((voff)[_i]), "s"((const char*)(gbase)) : "m0", "memory"); } while (0)
; #define PG8_WAIT_V(n) asm volatile("s_waitcnt vmcnt(" #n ")" ::: "memory")
; #define PG8_WAIT_L(n) asm volatile("s_waitcnt lgkmcnt(" #n ")" ::: "memory")
; #define PG8_BAR __builtin_amdgcn_s_barrier()
; #define PG8_SCHED __builtin_amdgcn_sched_barrier(0)
; template <class Epi, class Sched, bool F8 = false, bool MID = false, bool GATHER = false>
; __device__ __forceinline__ void gemm_phase(LAS unsigned char* lds, const Gemm g, const Sched& S, const Epi& E) {
;     ...
;             PG8_LDB(B0, 1, 0); PG8_LDB(B1, 1, 1); PG8_SCHED; PG8_LDA(At, 1, 0); PG8_STAGE(PG8_SA(0, 1), a2, xA1);
;             PG8_WAIT_V(8); PG8_WAIT_L(0); PG8_BAR; PG8_MMA(0, 0, At, B0); PG8_MMA(0, 1, At, B1); PG8_BAR; PG8_SCHED;
;             PG8_LDA(At, 1, 1); PG8_STAGE(PG8_SB(1, 0), b3, voffB); PG8_STAGE(PG8_SB(1, 1), b3 + hstepB, voffB); PG8_STAGE(PG8_SA(1, 0), a3, xA0);
;             PG8_WAIT_V(8); PG8_WAIT_L(0); PG8_BAR; PG8_MMA(1, 0, At, B0); PG8_MMA(1, 1, At, B1); PG8_BAR; PG8_SCHED;
	ds_read_b128 v[2:5], v174
	ds_read_b128 v[6:9], v174 offset:1024
	ds_read_b128 v[10:13], v174 offset:2048
	ds_read_b128 v[14:17], v174 offset:3072
	ds_read_b128 v[18:21], v175
	ds_read_b128 v[22:25], v175 offset:1024
	ds_read_b128 v[26:29], v175 offset:2048
	ds_read_b128 v[30:33], v175 offset:3072
	ds_read_b128 v[176:179], v171 offset:32768
	ds_read_b128 v[180:183], v171 offset:33792
	ds_read_b128 v[184:187], v171 offset:34816
	ds_read_b128 v[188:191], v171 offset:35840
	ds_read_b128 v[192:195], v171 offset:36864
	ds_read_b128 v[196:199], v171 offset:37888
	ds_read_b128 v[200:203], v171 offset:38912
	ds_read_b128 v[204:207], v171 offset:39936
	s_mov_b32 m0, s66
	s_nop 0
	global_load_lds_dwordx4 v162, s[60:61]
	s_nop 0
	s_mov_b32 m0, s67
	s_nop 0
	global_load_lds_dwordx4 v167, s[60:61]
	s_waitcnt vmcnt(8)
	s_waitcnt lgkmcnt(0)
	s_barrier
	s_setprio 1
	s_waitcnt lgkmcnt(6)
	v_mfma_scale_f32_16x16x128_f8f6f4 v[158:161], v[2:9], v[176:183], v[158:161], v172, v173 op_sel_hi:[0,0,0]
	v_mfma_scale_f32_16x16x128_f8f6f4 v[154:157], v[10:17], v[176:183], v[154:157], v172, v173 op_sel_hi:[0,0,0]
	s_waitcnt lgkmcnt(4)
	v_mfma_scale_f32_16x16x128_f8f6f4 v[150:153], v[2:9], v[184:191], v[150:153], v172, v173 op_sel_hi:[0,0,0]
	v_mfma_scale_f32_16x16x128_f8f6f4 v[142:145], v[10:17], v[184:191], v[142:145], v172, v173 op_sel_hi:[0,0,0]
	s_waitcnt lgkmcnt(2)
	v_mfma_scale_f32_16x16x128_f8f6f4 v[134:137], v[2:9], v[192:199], v[134:137], v172, v173 op_sel_hi:[0,0,0]
	v_mfma_scale_f32_16x16x128_f8f6f4 v[126:129], v[10:17], v[192:199], v[126:129], v172, v173 op_sel_hi:[0,0,0]
	s_waitcnt lgkmcnt(0)
	v_mfma_scale_f32_16x16x128_f8f6f4 v[118:121], v[2:9], v[200:207], v[118:121], v172, v173 op_sel_hi:[0,0,0]
	v_mfma_scale_f32_16x16x128_f8f6f4 v[110:113], v[10:17], v[200:207], v[110:113], v172, v173 op_sel_hi:[0,0,0]
	s_setprio 0
	s_setprio 1
	v_mfma_scale_f32_16x16x128_f8f6f4 v[146:149], v[18:25], v[176:183], v[146:149], v172, v173 op_sel_hi:[0,0,0]
	v_mfma_scale_f32_16x16x128_f8f6f4 v[138:141], v[26:33], v[176:183], v[138:141], v172, v173 op_sel_hi:[0,0,0]
	v_mfma_scale_f32_16x16x128_f8f6f4 v[130:133], v[18:25], v[184:191], v[130:133], v172, v173 op_sel_hi:[0,0,0]
	v_mfma_scale_f32_16x16x128_f8f6f4 v[122:125], v[26:33], v[184:191], v[122:125], v172, v173 op_sel_hi:[0,0,0]
	v_mfma_scale_f32_16x16x128_f8f6f4 v[114:117], v[18:25], v[192:199], v[114:117], v172, v173 op_sel_hi:[0,0,0]
	v_mfma_scale_f32_16x16x128_f8f6f4 v[106:109], v[26:33], v[192:199], v[106:109], v172, v173 op_sel_hi:[0,0,0]
	v_mfma_scale_f32_16x16x128_f8f6f4 v[102:105], v[18:25], v[200:207], v[102:105], v172, v173 op_sel_hi:[0,0,0]
	v_mfma_scale_f32_16x16x128_f8f6f4 v[98:101], v[26:33], v[200:207], v[98:101], v172, v173 op_sel_hi:[0,0,0]
	s_setprio 0
	s_barrier
	ds_read_b128 v[176:179], v171 offset:49152
	ds_read_b128 v[180:183], v171 offset:50176
	ds_read_b128 v[184:187], v171 offset:51200
	ds_read_b128 v[188:191], v171 offset:52224
	ds_read_b128 v[192:195], v171 offset:53248
	ds_read_b128 v[196:199], v171 offset:54272
	ds_read_b128 v[200:203], v171 offset:55296
	ds_read_b128 v[204:207], v171 offset:56320
	s_add_u32 s54, s56, 0x80
	s_addc_u32 s55, s57, 0
	s_mov_b32 m0, s70
	s_nop 0
	global_load_lds_dwordx4 v163, s[54:55]
	s_nop 0
	s_mov_b32 m0, s71
	s_nop 0
	global_load_lds_dwordx4 v168, s[54:55]
	s_add_u32 s54, s56, 0x40080
	s_addc_u32 s55, s57, 0
	s_mov_b32 m0, s75
	s_nop 0
	global_load_lds_dwordx4 v163, s[54:55]
	s_nop 0
	s_mov_b32 m0, s76
	s_nop 0
	global_load_lds_dwordx4 v168, s[54:55]
	s_nop 0
	s_waitcnt vmcnt(6)
	s_waitcnt lgkmcnt(0)
	s_barrier
	s_setprio 1
	s_waitcnt lgkmcnt(6)
	v_mfma_scale_f32_16x16x128_f8f6f4 v[94:97], v[2:9], v[176:183], v[94:97], v172, v173 op_sel_hi:[0,0,0]
	v_mfma_scale_f32_16x16x128_f8f6f4 v[90:93], v[10:17], v[176:183], v[90:93], v172, v173 op_sel_hi:[0,0,0]
	s_mov_b32 m0, s72
	s_nop 0
	global_load_lds_dwordx4 v1, s[58:59]
	s_waitcnt lgkmcnt(4)
	v_mfma_scale_f32_16x16x128_f8f6f4 v[78:81], v[2:9], v[184:191], v[78:81], v172, v173 op_sel_hi:[0,0,0]
	v_mfma_scale_f32_16x16x128_f8f6f4 v[70:73], v[10:17], v[184:191], v[70:73], v172, v173 op_sel_hi:[0,0,0]
	s_mov_b32 m0, s73
	s_nop 0
	global_load_lds_dwordx4 v165, s[58:59]
	s_waitcnt lgkmcnt(2)
	v_mfma_scale_f32_16x16x128_f8f6f4 v[54:57], v[2:9], v[192:199], v[54:57], v172, v173 op_sel_hi:[0,0,0]
	v_mfma_scale_f32_16x16x128_f8f6f4 v[46:49], v[10:17], v[192:199], v[46:49], v172, v173 op_sel_hi:[0,0,0]
	s_waitcnt lgkmcnt(0)
	v_mfma_scale_f32_16x16x128_f8f6f4 v[38:41], v[2:9], v[200:207], v[38:41], v172, v173 op_sel_hi:[0,0,0]
	v_mfma_scale_f32_16x16x128_f8f6f4 v[34:37], v[10:17], v[200:207], v[34:37], v172, v173 op_sel_hi:[0,0,0]
	s_setprio 0
	s_setprio 1
	v_mfma_scale_f32_16x16x128_f8f6f4 v[74:77], v[18:25], v[176:183], v[74:77], v172, v173 op_sel_hi:[0,0,0]
	v_mfma_scale_f32_16x16x128_f8f6f4 v[62:65], v[26:33], v[176:183], v[62:65], v172, v173 op_sel_hi:[0,0,0]
	v_mfma_scale_f32_16x16x128_f8f6f4 v[50:53], v[18:25], v[184:191], v[50:53], v172, v173 op_sel_hi:[0,0,0]
	v_mfma_scale_f32_16x16x128_f8f6f4 v[42:45], v[26:33], v[184:191], v[42:45], v172, v173 op_sel_hi:[0,0,0]
	v_mfma_scale_f32_16x16x128_f8f6f4 v[86:89], v[18:25], v[192:199], v[86:89], v172, v173 op_sel_hi:[0,0,0]
	v_mfma_scale_f32_16x16x128_f8f6f4 v[82:85], v[26:33], v[192:199], v[82:85], v172, v173 op_sel_hi:[0,0,0]
	v_mfma_scale_f32_16x16x128_f8f6f4 v[66:69], v[18:25], v[200:207], v[66:69], v172, v173 op_sel_hi:[0,0,0]
	v_mfma_scale_f32_16x16x128_f8f6f4 v[58:61], v[26:33], v[200:207], v[58:61], v172, v173 op_sel_hi:[0,0,0]
	s_setprio 0
	s_barrier
	s_add_i32 s96, s96, 2
	s_add_u32 s94, s94, 0x100
	s_addc_u32 s95, s95, 0
	s_cmp_gt_u32 s96, 13
	s_mov_b64 s[54:55], s[52:53]
	s_cbranch_scc0 .LBB0_1931
	s_and_b64 vcc, exec, s[10:11]
	s_cbranch_vccz .LBB0_1934
	s_barrier

; #define PG8_STAGE(bufoff, gbase, voff) do { _Pragma("unroll") for (int _i = 0; _i < 2; ++_i) \
;         asm volatile("s_mov_b32 m0, %0\n\ts_nop 0\n\tglobal_load_lds_dwordx4 %1, %2" :: "s"(ldsb + (unsigned)(bufoff) + ldsw + _i * 8192u), "v"((voff)[_i]), "s"((const char*)(gbase)) : "m0", "memory"); } while (0)
; #define PG8_WAIT_V(n) asm volatile("s_waitcnt vmcnt(" #n ")" ::: "memory")
; #define PG8_WAIT_L(n) asm volatile("s_waitcnt lgkmcnt(" #n ")" ::: "memory")
; #define PG8_BAR __builtin_amdgcn_s_barrier()
; #define PG8_SCHED __builtin_amdgcn_sched_barrier(0)
; template <class Epi, class Sched, bool F8 = false, bool MID = false, bool GATHER = false>
; __device__ __forceinline__ void gemm_phase(LAS unsigned char* lds, const Gemm g, const Sched& S, const Epi& E) {
;     ...
;             const char* a1 = cA + (size_t)(t + 1) * kstep;
;             const char* a2 = last ? nA : cA + (size_t)(t + 2) * kstep; const char* b2 = last ? nB : cB + (size_t)(t + 2) * kstep;
;             const char* a3 = a2 + kstep; const char* b3 = b2 + kstep;
;             unsigned xA0[2], xA1[2];
; #pragma unroll
;             for (int i = 0; i < 2; ++i) { xA0[i] = last ? nvA0[i] : voffA[i]; xA1[i] = last ? nvA1[i] : voffA1[i]; }
;             if constexpr (MID) { if (t == (nt >> 1)) { if constexpr (F8) asm volatile("s_nop 15\n\ts_nop 15" ::: "memory"); int l_; asm volatile("v_mbcnt_lo_u32_b32 %0, -1, 0\n\tv_mbcnt_hi_u32_b32 %0, -1, %0" : "=v"(l_)); E.mid(acc, cur, wr, wc, l_ & 15, l_ >> 4); if constexpr (F8) asm volatile("s_nop 7" ::: "memory"); } }
;             PG8_LDB(B0, 0, 0); PG8_LDB(B1, 0, 1); PG8_SCHED; PG8_LDA(At, 0, 0); PG8_STAGE(PG8_SA(1, 1), a1, voffA1);
;             PG8_WAIT_V(8); PG8_WAIT_L(0); PG8_BAR; PG8_MMA(0, 0, At, B0); PG8_MMA(0, 1, At, B1); PG8_BAR; PG8_SCHED;
;             PG8_LDA(At, 0, 1); PG8_STAGE(PG8_SB(0, 0), b2, voffB); PG8_STAGE(PG8_SB(0, 1), b2 + hstepB, voffB); PG8_STAGE(PG8_SA(0, 0), a2, xA0);
;             PG8_WAIT_V(8); PG8_WAIT_L(0); PG8_BAR; PG8_MMA(1, 0, At, B0); PG8_MMA(1, 1, At, B1); PG8_BAR; PG8_SCHED;
.LBB0_2474:
	s_add_u32 s22, s34, s64
	s_addc_u32 s23, s35, s65
	s_add_u32 s57, s22, 0x100
	s_addc_u32 s68, s23, 0
	s_add_u32 s66, s16, s64
	s_addc_u32 s67, s17, s65
	s_add_u32 s69, s66, 0x100
	s_addc_u32 s83, s67, 0
	v_add_u32_e32 v2, 0x10000, v172
	v_add_u32_e32 v14, 0x14000, v172
	s_cmp_eq_u32 s13, 12
	ds_read_b128 v[18:21], v2
	ds_read_b128 v[22:25], v2 offset:1024
	ds_read_b128 v[26:29], v2 offset:2048
	ds_read_b128 v[30:33], v2 offset:3072
	ds_read_b128 v[2:5], v14
	ds_read_b128 v[6:9], v14 offset:1024
	ds_read_b128 v[10:13], v14 offset:2048
	ds_read_b128 v[14:17], v14 offset:3072
	s_cselect_b64 vcc, -1, 0
	s_and_b64 s[66:67], vcc, exec
	s_cselect_b32 s70, s62, s57
	s_cselect_b32 s71, s63, s68
	s_cselect_b32 s66, s60, s69
	s_cselect_b32 s67, s61, s83
	s_add_u32 s68, s70, 0x80
	s_addc_u32 s69, s71, 0
	s_add_u32 s22, s22, 0x80
	v_cndmask_b32_e32 v181, v169, v177, vcc
	v_cndmask_b32_e32 v183, v168, v178, vcc
	v_cndmask_b32_e32 v182, v171, v179, vcc
	v_cndmask_b32_e32 v216, v170, v180, vcc
	s_addc_u32 s23, s23, 0
	ds_read_b128 v[184:187], v173
	ds_read_b128 v[188:191], v173 offset:1024
	ds_read_b128 v[192:195], v173 offset:2048
	ds_read_b128 v[196:199], v173 offset:3072
	ds_read_b128 v[200:203], v173 offset:4096
	ds_read_b128 v[204:207], v173 offset:5120
	ds_read_b128 v[208:211], v173 offset:6144
	ds_read_b128 v[212:215], v173 offset:7168
	s_mov_b32 m0, s95
	s_nop 0
	global_load_lds_dwordx4 v168, s[22:23]
	s_nop 0
	s_mov_b32 m0, s96
	s_nop 0
	global_load_lds_dwordx4 v170, s[22:23]
	s_waitcnt vmcnt(8)
	s_waitcnt lgkmcnt(0)
	s_barrier
	s_setprio 1
	s_waitcnt lgkmcnt(6)
	v_mfma_scale_f32_16x16x128_f8f6f4 v[158:161], v[18:25], v[184:191], v[158:161], v174, v175 op_sel_hi:[0,0,0]
	v_mfma_scale_f32_16x16x128_f8f6f4 v[154:157], v[26:33], v[184:191], v[154:157], v174, v175 op_sel_hi:[0,0,0]
	s_waitcnt lgkmcnt(4)
	v_mfma_scale_f32_16x16x128_f8f6f4 v[150:153], v[18:25], v[192:199], v[150:153], v174, v175 op_sel_hi:[0,0,0]
	v_mfma_scale_f32_16x16x128_f8f6f4 v[146:149], v[26:33], v[192:199], v[146:149], v174, v175 op_sel_hi:[0,0,0]
	s_waitcnt lgkmcnt(2)
	v_mfma_scale_f32_16x16x128_f8f6f4 v[142:145], v[18:25], v[200:207], v[142:145], v174, v175 op_sel_hi:[0,0,0]
	v_mfma_scale_f32_16x16x128_f8f6f4 v[138:141], v[26:33], v[200:207], v[138:141], v174, v175 op_sel_hi:[0,0,0]
	s_waitcnt lgkmcnt(0)
	v_mfma_scale_f32_16x16x128_f8f6f4 v[134:137], v[18:25], v[208:215], v[134:137], v174, v175 op_sel_hi:[0,0,0]
	v_mfma_scale_f32_16x16x128_f8f6f4 v[130:133], v[26:33], v[208:215], v[130:133], v174, v175 op_sel_hi:[0,0,0]
	s_setprio 0
	s_setprio 1
	v_mfma_scale_f32_16x16x128_f8f6f4 v[126:129], v[2:9], v[184:191], v[126:129], v174, v175 op_sel_hi:[0,0,0]
	v_mfma_scale_f32_16x16x128_f8f6f4 v[122:125], v[10:17], v[184:191], v[122:125], v174, v175 op_sel_hi:[0,0,0]
	v_mfma_scale_f32_16x16x128_f8f6f4 v[118:121], v[2:9], v[192:199], v[118:121], v174, v175 op_sel_hi:[0,0,0]
	v_mfma_scale_f32_16x16x128_f8f6f4 v[114:117], v[10:17], v[192:199], v[114:117], v174, v175 op_sel_hi:[0,0,0]
	v_mfma_scale_f32_16x16x128_f8f6f4 v[110:113], v[2:9], v[200:207], v[110:113], v174, v175 op_sel_hi:[0,0,0]
	v_mfma_scale_f32_16x16x128_f8f6f4 v[106:109], v[10:17], v[200:207], v[106:109], v174, v175 op_sel_hi:[0,0,0]
	v_mfma_scale_f32_16x16x128_f8f6f4 v[102:105], v[2:9], v[208:215], v[102:105], v174, v175 op_sel_hi:[0,0,0]
	v_mfma_scale_f32_16x16x128_f8f6f4 v[98:101], v[10:17], v[208:215], v[98:101], v174, v175 op_sel_hi:[0,0,0]
	s_setprio 0
	s_barrier
	ds_read_b128 v[184:187], v173 offset:16384
	ds_read_b128 v[188:191], v173 offset:17408
	ds_read_b128 v[192:195], v173 offset:18432
	ds_read_b128 v[196:199], v173 offset:19456
	ds_read_b128 v[200:203], v173 offset:20480
	ds_read_b128 v[204:207], v173 offset:21504
	ds_read_b128 v[208:211], v173 offset:22528
	ds_read_b128 v[212:215], v173 offset:23552
	s_mov_b32 m0, s74
	s_nop 0
	global_load_lds_dwordx4 v163, s[66:67]
	s_add_u32 s22, s66, 0x40000
	s_mov_b32 m0, s75
	s_nop 0
	global_load_lds_dwordx4 v167, s[66:67]
	s_addc_u32 s23, s67, 0
	s_mov_b32 m0, s76
	s_nop 0
	global_load_lds_dwordx4 v163, s[22:23]
	s_nop 0
	s_mov_b32 m0, s78
	s_nop 0
	global_load_lds_dwordx4 v167, s[22:23]
	s_nop 0
	s_waitcnt vmcnt(6)
	s_waitcnt lgkmcnt(0)
	s_barrier
	s_setprio 1
	s_waitcnt lgkmcnt(6)
	v_mfma_scale_f32_16x16x128_f8f6f4 v[94:97], v[18:25], v[184:191], v[94:97], v174, v175 op_sel_hi:[0,0,0]
	v_mfma_scale_f32_16x16x128_f8f6f4 v[90:93], v[26:33], v[184:191], v[90:93], v174, v175 op_sel_hi:[0,0,0]
	s_mov_b32 m0, s73
	s_nop 0
	global_load_lds_dwordx4 v181, s[70:71]
	s_waitcnt lgkmcnt(4)
	v_mfma_scale_f32_16x16x128_f8f6f4 v[86:89], v[18:25], v[192:199], v[86:89], v174, v175 op_sel_hi:[0,0,0]
	v_mfma_scale_f32_16x16x128_f8f6f4 v[82:85], v[26:33], v[192:199], v[82:85], v174, v175 op_sel_hi:[0,0,0]
	s_mov_b32 m0, s79
	s_nop 0
	global_load_lds_dwordx4 v182, s[70:71]
	s_waitcnt lgkmcnt(2)
	v_mfma_scale_f32_16x16x128_f8f6f4 v[78:81], v[18:25], v[200:207], v[78:81], v174, v175 op_sel_hi:[0,0,0]
	v_mfma_scale_f32_16x16x128_f8f6f4 v[74:77], v[26:33], v[200:207], v[74:77], v174, v175 op_sel_hi:[0,0,0]
	s_waitcnt lgkmcnt(0)
	v_mfma_scale_f32_16x16x128_f8f6f4 v[70:73], v[18:25], v[208:215], v[70:73], v174, v175 op_sel_hi:[0,0,0]
	v_mfma_scale_f32_16x16x128_f8f6f4 v[66:69], v[26:33], v[208:215], v[66:69], v174, v175 op_sel_hi:[0,0,0]
	s_setprio 0
	s_setprio 1
	v_mfma_scale_f32_16x16x128_f8f6f4 v[62:65], v[2:9], v[184:191], v[62:65], v174, v175 op_sel_hi:[0,0,0]
	v_mfma_scale_f32_16x16x128_f8f6f4 v[58:61], v[10:17], v[184:191], v[58:61], v174, v175 op_sel_hi:[0,0,0]
	v_mfma_scale_f32_16x16x128_f8f6f4 v[54:57], v[2:9], v[192:199], v[54:57], v174, v175 op_sel_hi:[0,0,0]
	v_mfma_scale_f32_16x16x128_f8f6f4 v[50:53], v[10:17], v[192:199], v[50:53], v174, v175 op_sel_hi:[0,0,0]
	v_mfma_scale_f32_16x16x128_f8f6f4 v[46:49], v[2:9], v[200:207], v[46:49], v174, v175 op_sel_hi:[0,0,0]
	v_mfma_scale_f32_16x16x128_f8f6f4 v[42:45], v[10:17], v[200:207], v[42:45], v174, v175 op_sel_hi:[0,0,0]
	v_mfma_scale_f32_16x16x128_f8f6f4 v[38:41], v[2:9], v[208:215], v[38:41], v174, v175 op_sel_hi:[0,0,0]
	v_mfma_scale_f32_16x16x128_f8f6f4 v[34:37], v[10:17], v[208:215], v[34:37], v174, v175 op_sel_hi:[0,0,0]
	s_setprio 0
	s_barrier
; #define PG8_STAGE(bufoff, gbase, voff) do { _Pragma("unroll") for (int _i = 0; _i < 2; ++_i) \
;         asm volatile("s_mov_b32 m0, %0\n\ts_nop 0\n\tglobal_load_lds_dwordx4 %1, %2" :: "s"(ldsb + (unsigned)(bufoff) + ldsw + _i * 8192u), "v"((voff)[_i]), "s"((const char*)(gbase)) : "m0", "memory"); } while (0)
; #define PG8_WAIT_V(n) asm volatile("s_waitcnt vmcnt(" #n ")" ::: "memory")
; #define PG8_WAIT_L(n) asm volatile("s_waitcnt lgkmcnt(" #n ")" ::: "memory")
; #define PG8_BAR __builtin_amdgcn_s_barrier()
; #define PG8_SCHED __builtin_amdgcn_sched_barrier(0)
; template <class Epi, class Sched, bool F8 = false, bool MID = false, bool GATHER = false>
; __device__ __forceinline__ void gemm_phase(LAS unsigned char* lds, const Gemm g, const Sched& S, const Epi& E) {
;     ...
;             PG8_LDB(B0, 1, 0); PG8_LDB(B1, 1, 1); PG8_SCHED; PG8_LDA(At, 1, 0); PG8_STAGE(PG8_SA(0, 1), a2, xA1);
;             PG8_WAIT_V(8); PG8_WAIT_L(0); PG8_BAR; PG8_MMA(0, 0, At, B0); PG8_MMA(0, 1, At, B1); PG8_BAR; PG8_SCHED;
;             PG8_LDA(At, 1, 1); PG8_STAGE(PG8_SB(1, 0), b3, voffB); PG8_STAGE(PG8_SB(1, 1), b3 + hstepB, voffB); PG8_STAGE(PG8_SA(1, 0), a3, xA0);
;             PG8_WAIT_V(8); PG8_WAIT_L(0); PG8_BAR; PG8_MMA(1, 0, At, B0); PG8_MMA(1, 1, At, B1); PG8_BAR; PG8_SCHED;
	v_add_u32_e32 v14, 0x18000, v172
	v_add_u32_e32 v30, 0x1c000, v172
	ds_read_b128 v[2:5], v14
	ds_read_b128 v[6:9], v14 offset:1024
	ds_read_b128 v[10:13], v14 offset:2048
	ds_read_b128 v[14:17], v14 offset:3072
	ds_read_b128 v[18:21], v30
	ds_read_b128 v[22:25], v30 offset:1024
	ds_read_b128 v[26:29], v30 offset:2048
	ds_read_b128 v[30:33], v30 offset:3072
	ds_read_b128 v[184:187], v173 offset:32768
	ds_read_b128 v[188:191], v173 offset:33792
	ds_read_b128 v[192:195], v173 offset:34816
	ds_read_b128 v[196:199], v173 offset:35840
	ds_read_b128 v[200:203], v173 offset:36864
	ds_read_b128 v[204:207], v173 offset:37888
	ds_read_b128 v[208:211], v173 offset:38912
	ds_read_b128 v[212:215], v173 offset:39936
	s_mov_b32 m0, s85
	s_nop 0
	global_load_lds_dwordx4 v183, s[70:71]
	s_nop 0
	s_mov_b32 m0, s86
	s_nop 0
	global_load_lds_dwordx4 v216, s[70:71]
	s_waitcnt vmcnt(8)
	s_waitcnt lgkmcnt(0)
	s_barrier
	s_setprio 1
	s_waitcnt lgkmcnt(6)
	v_mfma_scale_f32_16x16x128_f8f6f4 v[158:161], v[2:9], v[184:191], v[158:161], v174, v175 op_sel_hi:[0,0,0]
	v_mfma_scale_f32_16x16x128_f8f6f4 v[154:157], v[10:17], v[184:191], v[154:157], v174, v175 op_sel_hi:[0,0,0]
	s_waitcnt lgkmcnt(4)
	v_mfma_scale_f32_16x16x128_f8f6f4 v[150:153], v[2:9], v[192:199], v[150:153], v174, v175 op_sel_hi:[0,0,0]
	v_mfma_scale_f32_16x16x128_f8f6f4 v[146:149], v[10:17], v[192:199], v[146:149], v174, v175 op_sel_hi:[0,0,0]
	s_waitcnt lgkmcnt(2)
	v_mfma_scale_f32_16x16x128_f8f6f4 v[142:145], v[2:9], v[200:207], v[142:145], v174, v175 op_sel_hi:[0,0,0]
	v_mfma_scale_f32_16x16x128_f8f6f4 v[138:141], v[10:17], v[200:207], v[138:141], v174, v175 op_sel_hi:[0,0,0]
	s_waitcnt lgkmcnt(0)
	v_mfma_scale_f32_16x16x128_f8f6f4 v[134:137], v[2:9], v[208:215], v[134:137], v174, v175 op_sel_hi:[0,0,0]
	v_mfma_scale_f32_16x16x128_f8f6f4 v[130:133], v[10:17], v[208:215], v[130:133], v174, v175 op_sel_hi:[0,0,0]
	s_setprio 0
	s_setprio 1
	v_mfma_scale_f32_16x16x128_f8f6f4 v[126:129], v[18:25], v[184:191], v[126:129], v174, v175 op_sel_hi:[0,0,0]
	v_mfma_scale_f32_16x16x128_f8f6f4 v[122:125], v[26:33], v[184:191], v[122:125], v174, v175 op_sel_hi:[0,0,0]
	v_mfma_scale_f32_16x16x128_f8f6f4 v[118:121], v[18:25], v[192:199], v[118:121], v174, v175 op_sel_hi:[0,0,0]
	v_mfma_scale_f32_16x16x128_f8f6f4 v[114:117], v[26:33], v[192:199], v[114:117], v174, v175 op_sel_hi:[0,0,0]
	v_mfma_scale_f32_16x16x128_f8f6f4 v[110:113], v[18:25], v[200:207], v[110:113], v174, v175 op_sel_hi:[0,0,0]
	v_mfma_scale_f32_16x16x128_f8f6f4 v[106:109], v[26:33], v[200:207], v[106:109], v174, v175 op_sel_hi:[0,0,0]
	v_mfma_scale_f32_16x16x128_f8f6f4 v[102:105], v[18:25], v[208:215], v[102:105], v174, v175 op_sel_hi:[0,0,0]
	v_mfma_scale_f32_16x16x128_f8f6f4 v[98:101], v[26:33], v[208:215], v[98:101], v174, v175 op_sel_hi:[0,0,0]
	s_setprio 0
	s_barrier
	ds_read_b128 v[184:187], v173 offset:49152
	ds_read_b128 v[188:191], v173 offset:50176
	ds_read_b128 v[192:195], v173 offset:51200
	ds_read_b128 v[196:199], v173 offset:52224
	ds_read_b128 v[200:203], v173 offset:53248
	ds_read_b128 v[204:207], v173 offset:54272
	ds_read_b128 v[208:211], v173 offset:55296
	ds_read_b128 v[212:215], v173 offset:56320
	s_add_u32 s22, s66, 0x80
	s_addc_u32 s23, s67, 0
	s_mov_b32 m0, s89
	s_nop 0
	global_load_lds_dwordx4 v163, s[22:23]
	s_nop 0
	s_mov_b32 m0, s90
	s_nop 0
	global_load_lds_dwordx4 v167, s[22:23]
	s_add_u32 s22, s66, 0x40080
	s_addc_u32 s23, s67, 0
	s_mov_b32 m0, s93
	s_nop 0
	global_load_lds_dwordx4 v163, s[22:23]
	s_nop 0
	s_mov_b32 m0, s94
	s_nop 0
	global_load_lds_dwordx4 v167, s[22:23]
	s_nop 0
	s_waitcnt vmcnt(6)
	s_waitcnt lgkmcnt(0)
	s_barrier
	s_setprio 1
	s_waitcnt lgkmcnt(6)
	v_mfma_scale_f32_16x16x128_f8f6f4 v[94:97], v[2:9], v[184:191], v[94:97], v174, v175 op_sel_hi:[0,0,0]
	v_mfma_scale_f32_16x16x128_f8f6f4 v[90:93], v[10:17], v[184:191], v[90:93], v174, v175 op_sel_hi:[0,0,0]
	s_mov_b32 m0, s91
	s_nop 0
	global_load_lds_dwordx4 v181, s[68:69]
	s_waitcnt lgkmcnt(4)
	v_mfma_scale_f32_16x16x128_f8f6f4 v[86:89], v[2:9], v[192:199], v[86:89], v174, v175 op_sel_hi:[0,0,0]
	v_mfma_scale_f32_16x16x128_f8f6f4 v[82:85], v[10:17], v[192:199], v[82:85], v174, v175 op_sel_hi:[0,0,0]
	s_mov_b32 m0, s92
	s_nop 0
	global_load_lds_dwordx4 v182, s[68:69]
	s_waitcnt lgkmcnt(2)
	v_mfma_scale_f32_16x16x128_f8f6f4 v[78:81], v[2:9], v[200:207], v[78:81], v174, v175 op_sel_hi:[0,0,0]
	v_mfma_scale_f32_16x16x128_f8f6f4 v[74:77], v[10:17], v[200:207], v[74:77], v174, v175 op_sel_hi:[0,0,0]
	s_waitcnt lgkmcnt(0)
	v_mfma_scale_f32_16x16x128_f8f6f4 v[70:73], v[2:9], v[208:215], v[70:73], v174, v175 op_sel_hi:[0,0,0]
	v_mfma_scale_f32_16x16x128_f8f6f4 v[66:69], v[10:17], v[208:215], v[66:69], v174, v175 op_sel_hi:[0,0,0]
	s_setprio 0
	s_setprio 1
	v_mfma_scale_f32_16x16x128_f8f6f4 v[62:65], v[18:25], v[184:191], v[62:65], v174, v175 op_sel_hi:[0,0,0]
	v_mfma_scale_f32_16x16x128_f8f6f4 v[58:61], v[26:33], v[184:191], v[58:61], v174, v175 op_sel_hi:[0,0,0]
	v_mfma_scale_f32_16x16x128_f8f6f4 v[54:57], v[18:25], v[192:199], v[54:57], v174, v175 op_sel_hi:[0,0,0]
	v_mfma_scale_f32_16x16x128_f8f6f4 v[50:53], v[26:33], v[192:199], v[50:53], v174, v175 op_sel_hi:[0,0,0]
	v_mfma_scale_f32_16x16x128_f8f6f4 v[46:49], v[18:25], v[200:207], v[46:49], v174, v175 op_sel_hi:[0,0,0]
	v_mfma_scale_f32_16x16x128_f8f6f4 v[42:45], v[26:33], v[200:207], v[42:45], v174, v175 op_sel_hi:[0,0,0]
	v_mfma_scale_f32_16x16x128_f8f6f4 v[38:41], v[18:25], v[208:215], v[38:41], v174, v175 op_sel_hi:[0,0,0]
	v_mfma_scale_f32_16x16x128_f8f6f4 v[34:37], v[26:33], v[208:215], v[34:37], v174, v175 op_sel_hi:[0,0,0]
	s_setprio 0
	s_barrier
	s_add_i32 s13, s13, 2
	s_add_u32 s64, s64, 0x100
	s_addc_u32 s65, s65, 0
	s_cmp_gt_u32 s13, 13
	s_cbranch_scc0 .LBB0_2474
	s_and_b64 vcc, exec, s[54:55]
	s_cbranch_vccz .LBB0_2477
	s_barrier

; #define PG8_STAGE(bufoff, gbase, voff) do { _Pragma("unroll") for (int _i = 0; _i < 2; ++_i) \
;         asm volatile("s_mov_b32 m0, %0\n\ts_nop 0\n\tglobal_load_lds_dwordx4 %1, %2" :: "s"(ldsb + (unsigned)(bufoff) + ldsw + _i * 8192u), "v"((voff)[_i]), "s"((const char*)(gbase)) : "m0", "memory"); } while (0)
; #define PG8_WAIT_V(n) asm volatile("s_waitcnt vmcnt(" #n ")" ::: "memory")
; #define PG8_WAIT_L(n) asm volatile("s_waitcnt lgkmcnt(" #n ")" ::: "memory")
; #define PG8_BAR __builtin_amdgcn_s_barrier()
; #define PG8_SCHED __builtin_amdgcn_sched_barrier(0)
; template <class Epi, class Sched, bool F8 = false, bool MID = false, bool GATHER = false>
; __device__ __forceinline__ void gemm_phase(LAS unsigned char* lds, const Gemm g, const Sched& S, const Epi& E) {
;     ...
;             PG8_LDB(B0, 0, 0); PG8_LDB(B1, 0, 1); PG8_SCHED; PG8_LDA(At, 0, 0); PG8_STAGE(PG8_SA(1, 1), a1, voffA1);
;             PG8_WAIT_V(8); PG8_WAIT_L(0); PG8_BAR; PG8_MMA(0, 0, At, B0); PG8_MMA(0, 1, At, B1); PG8_BAR; PG8_SCHED;
;             PG8_LDA(At, 0, 1); PG8_STAGE(PG8_SB(0, 0), b2, voffB); PG8_STAGE(PG8_SB(0, 1), b2 + hstepB, voffB); PG8_STAGE(PG8_SA(0, 0), a2, xA0);
;             PG8_WAIT_V(8); PG8_WAIT_L(0); PG8_BAR; PG8_MMA(1, 0, At, B0); PG8_MMA(1, 1, At, B1); PG8_BAR; PG8_SCHED;
.LBB0_2557:
	ds_read_b128 v[18:21], v169
	ds_read_b128 v[22:25], v169 offset:1024
	ds_read_b128 v[26:29], v169 offset:2048
	ds_read_b128 v[30:33], v169 offset:3072
	ds_read_b128 v[2:5], v170
	ds_read_b128 v[6:9], v170 offset:1024
	ds_read_b128 v[10:13], v170 offset:2048
	ds_read_b128 v[14:17], v170 offset:3072
	s_add_u32 s64, s66, 0x100
	s_addc_u32 s65, s67, 0
	s_cmp_eq_u32 vcc_lo, 12
	s_cselect_b32 s72, s56, s64
	s_cselect_b32 s73, s57, s65
	s_cselect_b32 s68, s58, s55
	s_cselect_b32 s69, s59, s97
	s_add_u32 s70, s72, 0x80
	s_addc_u32 s71, s73, 0
	s_add_u32 s22, s66, 0x80
	s_addc_u32 s23, s67, 0
	ds_read_b128 v[176:179], v171
	ds_read_b128 v[180:183], v171 offset:1024
	ds_read_b128 v[184:187], v171 offset:2048
	ds_read_b128 v[188:191], v171 offset:3072
	ds_read_b128 v[192:195], v171 offset:4096
	ds_read_b128 v[196:199], v171 offset:5120
	ds_read_b128 v[200:203], v171 offset:6144
	ds_read_b128 v[204:207], v171 offset:7168
	s_mov_b32 m0, s89
	s_nop 0
	global_load_lds_dwordx4 v162, s[22:23]
	s_nop 0
	s_mov_b32 m0, s90
	s_nop 0
	global_load_lds_dwordx4 v167, s[22:23]
	s_waitcnt vmcnt(8)
	s_waitcnt lgkmcnt(0)
	s_barrier
	s_setprio 1
	s_waitcnt lgkmcnt(0)
	v_mfma_scale_f32_16x16x128_f8f6f4 v[158:161], v[18:25], v[176:183], v[158:161], v172, v173 op_sel_hi:[0,0,0]
	v_mfma_scale_f32_16x16x128_f8f6f4 v[154:157], v[26:33], v[176:183], v[154:157], v172, v173 op_sel_hi:[0,0,0]
	v_mfma_scale_f32_16x16x128_f8f6f4 v[150:153], v[18:25], v[184:191], v[150:153], v172, v173 op_sel_hi:[0,0,0]
	v_mfma_scale_f32_16x16x128_f8f6f4 v[146:149], v[26:33], v[184:191], v[146:149], v172, v173 op_sel_hi:[0,0,0]
	v_mfma_scale_f32_16x16x128_f8f6f4 v[142:145], v[18:25], v[192:199], v[142:145], v172, v173 op_sel_hi:[0,0,0]
	v_mfma_scale_f32_16x16x128_f8f6f4 v[122:125], v[26:33], v[192:199], v[122:125], v172, v173 op_sel_hi:[0,0,0]
	v_mfma_scale_f32_16x16x128_f8f6f4 v[114:117], v[18:25], v[200:207], v[114:117], v172, v173 op_sel_hi:[0,0,0]
	v_mfma_scale_f32_16x16x128_f8f6f4 v[106:109], v[26:33], v[200:207], v[106:109], v172, v173 op_sel_hi:[0,0,0]
	s_setprio 0
	s_setprio 1
	v_mfma_scale_f32_16x16x128_f8f6f4 v[138:141], v[2:9], v[176:183], v[138:141], v172, v173 op_sel_hi:[0,0,0]
	v_mfma_scale_f32_16x16x128_f8f6f4 v[134:137], v[10:17], v[176:183], v[134:137], v172, v173 op_sel_hi:[0,0,0]
	v_mfma_scale_f32_16x16x128_f8f6f4 v[130:133], v[2:9], v[184:191], v[130:133], v172, v173 op_sel_hi:[0,0,0]
	v_mfma_scale_f32_16x16x128_f8f6f4 v[126:129], v[10:17], v[184:191], v[126:129], v172, v173 op_sel_hi:[0,0,0]
	v_mfma_scale_f32_16x16x128_f8f6f4 v[118:121], v[2:9], v[192:199], v[118:121], v172, v173 op_sel_hi:[0,0,0]
	v_mfma_scale_f32_16x16x128_f8f6f4 v[110:113], v[10:17], v[192:199], v[110:113], v172, v173 op_sel_hi:[0,0,0]
	v_mfma_scale_f32_16x16x128_f8f6f4 v[102:105], v[2:9], v[200:207], v[102:105], v172, v173 op_sel_hi:[0,0,0]
	v_mfma_scale_f32_16x16x128_f8f6f4 v[98:101], v[10:17], v[200:207], v[98:101], v172, v173 op_sel_hi:[0,0,0]
	s_setprio 0
	s_barrier
	ds_read_b128 v[176:179], v171 offset:16384
	ds_read_b128 v[180:183], v171 offset:17408
	ds_read_b128 v[184:187], v171 offset:18432
	ds_read_b128 v[188:191], v171 offset:19456
	ds_read_b128 v[192:195], v171 offset:20480
	ds_read_b128 v[196:199], v171 offset:21504
	ds_read_b128 v[200:203], v171 offset:22528
	ds_read_b128 v[204:207], v171 offset:23552
	s_mov_b32 m0, s26
	s_nop 0
	global_load_lds_dwordx4 v163, s[68:69]
	s_add_u32 s22, s68, 0x40000
	s_mov_b32 m0, s27
	s_nop 0
	global_load_lds_dwordx4 v168, s[68:69]
	s_addc_u32 s23, s69, 0
	s_mov_b32 m0, s39
	s_nop 0
	global_load_lds_dwordx4 v163, s[22:23]
	s_nop 0
	s_mov_b32 m0, s41
	s_nop 0
	global_load_lds_dwordx4 v168, s[22:23]
	s_nop 0
	s_waitcnt vmcnt(6)
	s_waitcnt lgkmcnt(0)
	s_barrier
	s_setprio 1
	s_waitcnt lgkmcnt(6)
	v_mfma_scale_f32_16x16x128_f8f6f4 v[94:97], v[18:25], v[176:183], v[94:97], v172, v173 op_sel_hi:[0,0,0]
	v_mfma_scale_f32_16x16x128_f8f6f4 v[90:93], v[26:33], v[176:183], v[90:93], v172, v173 op_sel_hi:[0,0,0]
	s_mov_b32 m0, s17
	s_nop 0
	global_load_lds_dwordx4 v1, s[72:73]
	s_waitcnt lgkmcnt(4)
	v_mfma_scale_f32_16x16x128_f8f6f4 v[82:85], v[18:25], v[184:191], v[82:85], v172, v173 op_sel_hi:[0,0,0]
	v_mfma_scale_f32_16x16x128_f8f6f4 v[70:73], v[26:33], v[184:191], v[70:73], v172, v173 op_sel_hi:[0,0,0]
	s_mov_b32 m0, s74
	s_nop 0
	global_load_lds_dwordx4 v165, s[72:73]
	s_waitcnt lgkmcnt(2)
	v_mfma_scale_f32_16x16x128_f8f6f4 v[54:57], v[18:25], v[192:199], v[54:57], v172, v173 op_sel_hi:[0,0,0]
	v_mfma_scale_f32_16x16x128_f8f6f4 v[42:45], v[26:33], v[192:199], v[42:45], v172, v173 op_sel_hi:[0,0,0]
	s_waitcnt lgkmcnt(0)
	v_mfma_scale_f32_16x16x128_f8f6f4 v[38:41], v[18:25], v[200:207], v[38:41], v172, v173 op_sel_hi:[0,0,0]
	v_mfma_scale_f32_16x16x128_f8f6f4 v[34:37], v[26:33], v[200:207], v[34:37], v172, v173 op_sel_hi:[0,0,0]
	s_setprio 0
	s_setprio 1
	v_mfma_scale_f32_16x16x128_f8f6f4 v[86:89], v[2:9], v[176:183], v[86:89], v172, v173 op_sel_hi:[0,0,0]
	v_mfma_scale_f32_16x16x128_f8f6f4 v[78:81], v[10:17], v[176:183], v[78:81], v172, v173 op_sel_hi:[0,0,0]
	v_mfma_scale_f32_16x16x128_f8f6f4 v[62:65], v[2:9], v[184:191], v[62:65], v172, v173 op_sel_hi:[0,0,0]
	v_mfma_scale_f32_16x16x128_f8f6f4 v[46:49], v[10:17], v[184:191], v[46:49], v172, v173 op_sel_hi:[0,0,0]
	v_mfma_scale_f32_16x16x128_f8f6f4 v[74:77], v[2:9], v[192:199], v[74:77], v172, v173 op_sel_hi:[0,0,0]
	v_mfma_scale_f32_16x16x128_f8f6f4 v[66:69], v[10:17], v[192:199], v[66:69], v172, v173 op_sel_hi:[0,0,0]
	v_mfma_scale_f32_16x16x128_f8f6f4 v[58:61], v[2:9], v[200:207], v[58:61], v172, v173 op_sel_hi:[0,0,0]
	v_mfma_scale_f32_16x16x128_f8f6f4 v[50:53], v[10:17], v[200:207], v[50:53], v172, v173 op_sel_hi:[0,0,0]
	s_setprio 0
	s_barrier
; #define PG8_STAGE(bufoff, gbase, voff) do { _Pragma("unroll") for (int _i = 0; _i < 2; ++_i) \
;         asm volatile("s_mov_b32 m0, %0\n\ts_nop 0\n\tglobal_load_lds_dwordx4 %1, %2" :: "s"(ldsb + (unsigned)(bufoff) + ldsw + _i * 8192u), "v"((voff)[_i]), "s"((const char*)(gbase)) : "m0", "memory"); } while (0)
; #define PG8_WAIT_V(n) asm volatile("s_waitcnt vmcnt(" #n ")" ::: "memory")
; #define PG8_WAIT_L(n) asm volatile("s_waitcnt lgkmcnt(" #n ")" ::: "memory")
; #define PG8_BAR __builtin_amdgcn_s_barrier()
; #define PG8_SCHED __builtin_amdgcn_sched_barrier(0)
; template <class Epi, class Sched, bool F8 = false, bool MID = false, bool GATHER = false>
; __device__ __forceinline__ void gemm_phase(LAS unsigned char* lds, const Gemm g, const Sched& S, const Epi& E) {
;     ...
;             PG8_LDB(B0, 1, 0); PG8_LDB(B1, 1, 1); PG8_SCHED; PG8_LDA(At, 1, 0); PG8_STAGE(PG8_SA(0, 1), a2, xA1);
;             PG8_WAIT_V(8); PG8_WAIT_L(0); PG8_BAR; PG8_MMA(0, 0, At, B0); PG8_MMA(0, 1, At, B1); PG8_BAR; PG8_SCHED;
;             PG8_LDA(At, 1, 1); PG8_STAGE(PG8_SB(1, 0), b3, voffB); PG8_STAGE(PG8_SB(1, 1), b3 + hstepB, voffB); PG8_STAGE(PG8_SA(1, 0), a3, xA0);
;             PG8_WAIT_V(8); PG8_WAIT_L(0); PG8_BAR; PG8_MMA(1, 0, At, B0); PG8_MMA(1, 1, At, B1); PG8_BAR; PG8_SCHED;
	ds_read_b128 v[2:5], v174
	ds_read_b128 v[6:9], v174 offset:1024
	ds_read_b128 v[10:13], v174 offset:2048
	ds_read_b128 v[14:17], v174 offset:3072
	ds_read_b128 v[18:21], v175
	ds_read_b128 v[22:25], v175 offset:1024
	ds_read_b128 v[26:29], v175 offset:2048
	ds_read_b128 v[30:33], v175 offset:3072
	ds_read_b128 v[176:179], v171 offset:32768
	ds_read_b128 v[180:183], v171 offset:33792
	ds_read_b128 v[184:187], v171 offset:34816
	ds_read_b128 v[188:191], v171 offset:35840
	ds_read_b128 v[192:195], v171 offset:36864
	ds_read_b128 v[196:199], v171 offset:37888
	ds_read_b128 v[200:203], v171 offset:38912
	ds_read_b128 v[204:207], v171 offset:39936
	s_mov_b32 m0, s75
	s_nop 0
	global_load_lds_dwordx4 v162, s[72:73]
	s_nop 0
	s_mov_b32 m0, s76
	s_nop 0
	global_load_lds_dwordx4 v167, s[72:73]
	s_waitcnt vmcnt(8)
	s_waitcnt lgkmcnt(0)
	s_barrier
	s_setprio 1
	s_waitcnt lgkmcnt(6)
	v_mfma_scale_f32_16x16x128_f8f6f4 v[158:161], v[2:9], v[176:183], v[158:161], v172, v173 op_sel_hi:[0,0,0]
	v_mfma_scale_f32_16x16x128_f8f6f4 v[154:157], v[10:17], v[176:183], v[154:157], v172, v173 op_sel_hi:[0,0,0]
	s_waitcnt lgkmcnt(4)
	v_mfma_scale_f32_16x16x128_f8f6f4 v[150:153], v[2:9], v[184:191], v[150:153], v172, v173 op_sel_hi:[0,0,0]
	v_mfma_scale_f32_16x16x128_f8f6f4 v[146:149], v[10:17], v[184:191], v[146:149], v172, v173 op_sel_hi:[0,0,0]
	s_waitcnt lgkmcnt(2)
	v_mfma_scale_f32_16x16x128_f8f6f4 v[142:145], v[2:9], v[192:199], v[142:145], v172, v173 op_sel_hi:[0,0,0]
	v_mfma_scale_f32_16x16x128_f8f6f4 v[122:125], v[10:17], v[192:199], v[122:125], v172, v173 op_sel_hi:[0,0,0]
	s_waitcnt lgkmcnt(0)
	v_mfma_scale_f32_16x16x128_f8f6f4 v[114:117], v[2:9], v[200:207], v[114:117], v172, v173 op_sel_hi:[0,0,0]
	v_mfma_scale_f32_16x16x128_f8f6f4 v[106:109], v[10:17], v[200:207], v[106:109], v172, v173 op_sel_hi:[0,0,0]
	s_setprio 0
	s_setprio 1
	v_mfma_scale_f32_16x16x128_f8f6f4 v[138:141], v[18:25], v[176:183], v[138:141], v172, v173 op_sel_hi:[0,0,0]
	v_mfma_scale_f32_16x16x128_f8f6f4 v[134:137], v[26:33], v[176:183], v[134:137], v172, v173 op_sel_hi:[0,0,0]
	v_mfma_scale_f32_16x16x128_f8f6f4 v[130:133], v[18:25], v[184:191], v[130:133], v172, v173 op_sel_hi:[0,0,0]
	v_mfma_scale_f32_16x16x128_f8f6f4 v[126:129], v[26:33], v[184:191], v[126:129], v172, v173 op_sel_hi:[0,0,0]
	v_mfma_scale_f32_16x16x128_f8f6f4 v[118:121], v[18:25], v[192:199], v[118:121], v172, v173 op_sel_hi:[0,0,0]
	v_mfma_scale_f32_16x16x128_f8f6f4 v[110:113], v[26:33], v[192:199], v[110:113], v172, v173 op_sel_hi:[0,0,0]
	v_mfma_scale_f32_16x16x128_f8f6f4 v[102:105], v[18:25], v[200:207], v[102:105], v172, v173 op_sel_hi:[0,0,0]
	v_mfma_scale_f32_16x16x128_f8f6f4 v[98:101], v[26:33], v[200:207], v[98:101], v172, v173 op_sel_hi:[0,0,0]
	s_setprio 0
	s_barrier
	ds_read_b128 v[176:179], v171 offset:49152
	ds_read_b128 v[180:183], v171 offset:50176
	ds_read_b128 v[184:187], v171 offset:51200
	ds_read_b128 v[188:191], v171 offset:52224
	ds_read_b128 v[192:195], v171 offset:53248
	ds_read_b128 v[196:199], v171 offset:54272
	ds_read_b128 v[200:203], v171 offset:55296
	ds_read_b128 v[204:207], v171 offset:56320
	s_add_u32 s22, s68, 0x80
	s_addc_u32 s23, s69, 0
	s_mov_b32 m0, s80
	s_nop 0
	global_load_lds_dwordx4 v163, s[22:23]
	s_nop 0
	s_mov_b32 m0, s81
	s_nop 0
	global_load_lds_dwordx4 v168, s[22:23]
	s_add_u32 s22, s68, 0x40080
	s_addc_u32 s23, s69, 0
	s_mov_b32 m0, s87
	s_nop 0
	global_load_lds_dwordx4 v163, s[22:23]
	s_nop 0
	s_mov_b32 m0, s88
	s_nop 0
	global_load_lds_dwordx4 v168, s[22:23]
	s_nop 0
	s_waitcnt vmcnt(6)
	s_waitcnt lgkmcnt(0)
	s_barrier
	s_setprio 1
	s_waitcnt lgkmcnt(6)
	v_mfma_scale_f32_16x16x128_f8f6f4 v[94:97], v[2:9], v[176:183], v[94:97], v172, v173 op_sel_hi:[0,0,0]
	v_mfma_scale_f32_16x16x128_f8f6f4 v[90:93], v[10:17], v[176:183], v[90:93], v172, v173 op_sel_hi:[0,0,0]
	s_mov_b32 m0, s85
	s_nop 0
	global_load_lds_dwordx4 v1, s[70:71]
	s_waitcnt lgkmcnt(4)
	v_mfma_scale_f32_16x16x128_f8f6f4 v[82:85], v[2:9], v[184:191], v[82:85], v172, v173 op_sel_hi:[0,0,0]
	v_mfma_scale_f32_16x16x128_f8f6f4 v[70:73], v[10:17], v[184:191], v[70:73], v172, v173 op_sel_hi:[0,0,0]
	s_mov_b32 m0, s86
	s_nop 0
	global_load_lds_dwordx4 v165, s[70:71]
	s_waitcnt lgkmcnt(2)
	v_mfma_scale_f32_16x16x128_f8f6f4 v[54:57], v[2:9], v[192:199], v[54:57], v172, v173 op_sel_hi:[0,0,0]
	v_mfma_scale_f32_16x16x128_f8f6f4 v[42:45], v[10:17], v[192:199], v[42:45], v172, v173 op_sel_hi:[0,0,0]
	s_waitcnt lgkmcnt(0)
	v_mfma_scale_f32_16x16x128_f8f6f4 v[38:41], v[2:9], v[200:207], v[38:41], v172, v173 op_sel_hi:[0,0,0]
	v_mfma_scale_f32_16x16x128_f8f6f4 v[34:37], v[10:17], v[200:207], v[34:37], v172, v173 op_sel_hi:[0,0,0]
	s_setprio 0
	s_setprio 1
	v_mfma_scale_f32_16x16x128_f8f6f4 v[86:89], v[18:25], v[176:183], v[86:89], v172, v173 op_sel_hi:[0,0,0]
	v_mfma_scale_f32_16x16x128_f8f6f4 v[78:81], v[26:33], v[176:183], v[78:81], v172, v173 op_sel_hi:[0,0,0]
	v_mfma_scale_f32_16x16x128_f8f6f4 v[62:65], v[18:25], v[184:191], v[62:65], v172, v173 op_sel_hi:[0,0,0]
	v_mfma_scale_f32_16x16x128_f8f6f4 v[46:49], v[26:33], v[184:191], v[46:49], v172, v173 op_sel_hi:[0,0,0]
	v_mfma_scale_f32_16x16x128_f8f6f4 v[74:77], v[18:25], v[192:199], v[74:77], v172, v173 op_sel_hi:[0,0,0]
	v_mfma_scale_f32_16x16x128_f8f6f4 v[66:69], v[26:33], v[192:199], v[66:69], v172, v173 op_sel_hi:[0,0,0]
	v_mfma_scale_f32_16x16x128_f8f6f4 v[58:61], v[18:25], v[200:207], v[58:61], v172, v173 op_sel_hi:[0,0,0]
	v_mfma_scale_f32_16x16x128_f8f6f4 v[50:53], v[26:33], v[200:207], v[50:53], v172, v173 op_sel_hi:[0,0,0]
	s_setprio 0
	s_barrier
	s_add_i32 vcc_lo, vcc_lo, 2
	s_add_u32 s55, s55, 0x100
	s_addc_u32 s97, s97, 0
	s_cmp_gt_u32 vcc_lo, 13
	s_mov_b64 s[66:67], s[64:65]
	s_cbranch_scc0 .LBB0_2557
	s_and_b64 vcc, exec, s[12:13]
	s_cbranch_vccz .LBB0_2560
	s_barrier

; #define PG8_STAGE(bufoff, gbase, voff) do { _Pragma("unroll") for (int _i = 0; _i < 2; ++_i) \
;         asm volatile("s_mov_b32 m0, %0\n\ts_nop 0\n\tglobal_load_lds_dwordx4 %1, %2" :: "s"(ldsb + (unsigned)(bufoff) + ldsw + _i * 8192u), "v"((voff)[_i]), "s"((const char*)(gbase)) : "m0", "memory"); } while (0)
; #define PG8_WAIT_V(n) asm volatile("s_waitcnt vmcnt(" #n ")" ::: "memory")
; #define PG8_WAIT_L(n) asm volatile("s_waitcnt lgkmcnt(" #n ")" ::: "memory")
; #define PG8_BAR __builtin_amdgcn_s_barrier()
; #define PG8_SCHED __builtin_amdgcn_sched_barrier(0)
; template <class Epi, class Sched, bool F8 = false, bool MID = false, bool GATHER = false>
; __device__ __forceinline__ void gemm_phase(LAS unsigned char* lds, const Gemm g, const Sched& S, const Epi& E) {
;     ...
;             PG8_LDB(B0, 0, 0); PG8_LDB(B1, 0, 1); PG8_SCHED; PG8_LDA(At, 0, 0); PG8_STAGE(PG8_SA(1, 1), a1, voffA1);
;             PG8_WAIT_V(8); PG8_WAIT_L(0); PG8_BAR; PG8_MMA(0, 0, At, B0); PG8_MMA(0, 1, At, B1); PG8_BAR; PG8_SCHED;
;             PG8_LDA(At, 0, 1); PG8_STAGE(PG8_SB(0, 0), b2, voffB); PG8_STAGE(PG8_SB(0, 1), b2 + hstepB, voffB); PG8_STAGE(PG8_SA(0, 0), a2, xA0);
;             PG8_WAIT_V(8); PG8_WAIT_L(0); PG8_BAR; PG8_MMA(1, 0, At, B0); PG8_MMA(1, 1, At, B1); PG8_BAR; PG8_SCHED;
.LBB0_2753:
	ds_read_b128 v[16:19], v166
	ds_read_b128 v[20:23], v166 offset:1024
	ds_read_b128 v[24:27], v166 offset:2048
	ds_read_b128 v[28:31], v166 offset:3072
	ds_read_b128 v[0:3], v168
	ds_read_b128 v[4:7], v168 offset:1024
	ds_read_b128 v[8:11], v168 offset:2048
	ds_read_b128 v[12:15], v168 offset:3072
	s_add_u32 s48, s50, 0x100
	s_addc_u32 s49, s51, 0
	s_cmp_eq_u32 s90, 12
	s_cselect_b32 s56, s44, s48
	s_cselect_b32 s57, s45, s49
	s_cselect_b32 s52, s46, s88
	s_cselect_b32 s53, s47, s89
	s_add_u32 s54, s56, 0x80
	s_addc_u32 s55, s57, 0
	s_add_u32 s22, s50, 0x80
	s_addc_u32 s23, s51, 0
	ds_read_b128 v[174:177], v169
	ds_read_b128 v[178:181], v169 offset:1024
	ds_read_b128 v[182:185], v169 offset:2048
	ds_read_b128 v[186:189], v169 offset:3072
	ds_read_b128 v[190:193], v169 offset:4096
	ds_read_b128 v[194:197], v169 offset:5120
	ds_read_b128 v[198:201], v169 offset:6144
	ds_read_b128 v[202:205], v169 offset:7168
	s_mov_b32 m0, s75
	s_nop 0
	global_load_lds_dwordx4 v161, s[22:23]
	s_nop 0
	s_mov_b32 m0, s76
	s_nop 0
	global_load_lds_dwordx4 v165, s[22:23]
	s_waitcnt vmcnt(8)
	s_waitcnt lgkmcnt(0)
	s_barrier
	s_setprio 1
	s_waitcnt lgkmcnt(6)
	v_mfma_scale_f32_16x16x128_f8f6f4 v[156:159], v[16:23], v[174:181], v[156:159], v170, v171 op_sel_hi:[0,0,0]
	v_mfma_scale_f32_16x16x128_f8f6f4 v[152:155], v[24:31], v[174:181], v[152:155], v170, v171 op_sel_hi:[0,0,0]
	s_waitcnt lgkmcnt(4)
	v_mfma_scale_f32_16x16x128_f8f6f4 v[140:143], v[16:23], v[182:189], v[140:143], v170, v171 op_sel_hi:[0,0,0]
	v_mfma_scale_f32_16x16x128_f8f6f4 v[136:139], v[24:31], v[182:189], v[136:139], v170, v171 op_sel_hi:[0,0,0]
	s_waitcnt lgkmcnt(2)
	v_mfma_scale_f32_16x16x128_f8f6f4 v[124:127], v[16:23], v[190:197], v[124:127], v170, v171 op_sel_hi:[0,0,0]
	v_mfma_scale_f32_16x16x128_f8f6f4 v[120:123], v[24:31], v[190:197], v[120:123], v170, v171 op_sel_hi:[0,0,0]
	s_waitcnt lgkmcnt(0)
	v_mfma_scale_f32_16x16x128_f8f6f4 v[108:111], v[16:23], v[198:205], v[108:111], v170, v171 op_sel_hi:[0,0,0]
	v_mfma_scale_f32_16x16x128_f8f6f4 v[104:107], v[24:31], v[198:205], v[104:107], v170, v171 op_sel_hi:[0,0,0]
	s_setprio 0
	s_setprio 1
	v_mfma_scale_f32_16x16x128_f8f6f4 v[148:151], v[0:7], v[174:181], v[148:151], v170, v171 op_sel_hi:[0,0,0]
	v_mfma_scale_f32_16x16x128_f8f6f4 v[144:147], v[8:15], v[174:181], v[144:147], v170, v171 op_sel_hi:[0,0,0]
	v_mfma_scale_f32_16x16x128_f8f6f4 v[132:135], v[0:7], v[182:189], v[132:135], v170, v171 op_sel_hi:[0,0,0]
	v_mfma_scale_f32_16x16x128_f8f6f4 v[128:131], v[8:15], v[182:189], v[128:131], v170, v171 op_sel_hi:[0,0,0]
	v_mfma_scale_f32_16x16x128_f8f6f4 v[116:119], v[0:7], v[190:197], v[116:119], v170, v171 op_sel_hi:[0,0,0]
	v_mfma_scale_f32_16x16x128_f8f6f4 v[112:115], v[8:15], v[190:197], v[112:115], v170, v171 op_sel_hi:[0,0,0]
	v_mfma_scale_f32_16x16x128_f8f6f4 v[100:103], v[0:7], v[198:205], v[100:103], v170, v171 op_sel_hi:[0,0,0]
	v_mfma_scale_f32_16x16x128_f8f6f4 v[96:99], v[8:15], v[198:205], v[96:99], v170, v171 op_sel_hi:[0,0,0]
	s_setprio 0
	s_barrier
	ds_read_b128 v[174:177], v169 offset:16384
	ds_read_b128 v[178:181], v169 offset:17408
	ds_read_b128 v[182:185], v169 offset:18432
	ds_read_b128 v[186:189], v169 offset:19456
	ds_read_b128 v[190:193], v169 offset:20480
	ds_read_b128 v[194:197], v169 offset:21504
	ds_read_b128 v[198:201], v169 offset:22528
	ds_read_b128 v[202:205], v169 offset:23552
	s_mov_b32 m0, s60
	s_nop 0
	global_load_lds_dwordx4 v162, s[52:53]
	s_add_u32 s22, s52, 0x40000
	s_mov_b32 m0, s61
	s_nop 0
	global_load_lds_dwordx4 v167, s[52:53]
	s_addc_u32 s23, s53, 0
	s_mov_b32 m0, s62
	s_nop 0
	global_load_lds_dwordx4 v162, s[22:23]
	s_nop 0
	s_mov_b32 m0, s63
	s_nop 0
	global_load_lds_dwordx4 v167, s[22:23]
	s_nop 0
	s_waitcnt vmcnt(6)
	s_waitcnt lgkmcnt(0)
	s_barrier
	s_setprio 1
	s_waitcnt lgkmcnt(6)
	v_mfma_scale_f32_16x16x128_f8f6f4 v[92:95], v[16:23], v[174:181], v[92:95], v170, v171 op_sel_hi:[0,0,0]
	v_mfma_scale_f32_16x16x128_f8f6f4 v[88:91], v[24:31], v[174:181], v[88:91], v170, v171 op_sel_hi:[0,0,0]
	s_mov_b32 m0, s58
	s_nop 0
	global_load_lds_dwordx4 v160, s[56:57]
	s_waitcnt lgkmcnt(4)
	v_mfma_scale_f32_16x16x128_f8f6f4 v[76:79], v[16:23], v[182:189], v[76:79], v170, v171 op_sel_hi:[0,0,0]
	v_mfma_scale_f32_16x16x128_f8f6f4 v[72:75], v[24:31], v[182:189], v[72:75], v170, v171 op_sel_hi:[0,0,0]
	s_mov_b32 m0, s64
	s_nop 0
	global_load_lds_dwordx4 v163, s[56:57]
	s_waitcnt lgkmcnt(2)
	v_mfma_scale_f32_16x16x128_f8f6f4 v[52:55], v[16:23], v[190:197], v[52:55], v170, v171 op_sel_hi:[0,0,0]
	v_mfma_scale_f32_16x16x128_f8f6f4 v[48:51], v[24:31], v[190:197], v[48:51], v170, v171 op_sel_hi:[0,0,0]
	s_waitcnt lgkmcnt(0)
	v_mfma_scale_f32_16x16x128_f8f6f4 v[36:39], v[16:23], v[198:205], v[36:39], v170, v171 op_sel_hi:[0,0,0]
	v_mfma_scale_f32_16x16x128_f8f6f4 v[32:35], v[24:31], v[198:205], v[32:35], v170, v171 op_sel_hi:[0,0,0]
	s_setprio 0
	s_setprio 1
	v_mfma_scale_f32_16x16x128_f8f6f4 v[84:87], v[0:7], v[174:181], v[84:87], v170, v171 op_sel_hi:[0,0,0]
	v_mfma_scale_f32_16x16x128_f8f6f4 v[80:83], v[8:15], v[174:181], v[80:83], v170, v171 op_sel_hi:[0,0,0]
	v_mfma_scale_f32_16x16x128_f8f6f4 v[68:71], v[0:7], v[182:189], v[68:71], v170, v171 op_sel_hi:[0,0,0]
	v_mfma_scale_f32_16x16x128_f8f6f4 v[56:59], v[8:15], v[182:189], v[56:59], v170, v171 op_sel_hi:[0,0,0]
	v_mfma_scale_f32_16x16x128_f8f6f4 v[64:67], v[0:7], v[190:197], v[64:67], v170, v171 op_sel_hi:[0,0,0]
	v_mfma_scale_f32_16x16x128_f8f6f4 v[60:63], v[8:15], v[190:197], v[60:63], v170, v171 op_sel_hi:[0,0,0]
	v_mfma_scale_f32_16x16x128_f8f6f4 v[44:47], v[0:7], v[198:205], v[44:47], v170, v171 op_sel_hi:[0,0,0]
	v_mfma_scale_f32_16x16x128_f8f6f4 v[40:43], v[8:15], v[198:205], v[40:43], v170, v171 op_sel_hi:[0,0,0]
	s_setprio 0
	s_barrier
; #define PG8_STAGE(bufoff, gbase, voff) do { _Pragma("unroll") for (int _i = 0; _i < 2; ++_i) \
;         asm volatile("s_mov_b32 m0, %0\n\ts_nop 0\n\tglobal_load_lds_dwordx4 %1, %2" :: "s"(ldsb + (unsigned)(bufoff) + ldsw + _i * 8192u), "v"((voff)[_i]), "s"((const char*)(gbase)) : "m0", "memory"); } while (0)
; #define PG8_WAIT_V(n) asm volatile("s_waitcnt vmcnt(" #n ")" ::: "memory")
; #define PG8_WAIT_L(n) asm volatile("s_waitcnt lgkmcnt(" #n ")" ::: "memory")
; #define PG8_BAR __builtin_amdgcn_s_barrier()
; #define PG8_SCHED __builtin_amdgcn_sched_barrier(0)
; template <class Epi, class Sched, bool F8 = false, bool MID = false, bool GATHER = false>
; __device__ __forceinline__ void gemm_phase(LAS unsigned char* lds, const Gemm g, const Sched& S, const Epi& E) {
;     ...
;             PG8_LDB(B0, 1, 0); PG8_LDB(B1, 1, 1); PG8_SCHED; PG8_LDA(At, 1, 0); PG8_STAGE(PG8_SA(0, 1), a2, xA1);
;             PG8_WAIT_V(8); PG8_WAIT_L(0); PG8_BAR; PG8_MMA(0, 0, At, B0); PG8_MMA(0, 1, At, B1); PG8_BAR; PG8_SCHED;
;             PG8_LDA(At, 1, 1); PG8_STAGE(PG8_SB(1, 0), b3, voffB); PG8_STAGE(PG8_SB(1, 1), b3 + hstepB, voffB); PG8_STAGE(PG8_SA(1, 0), a3, xA0);
;             PG8_WAIT_V(8); PG8_WAIT_L(0); PG8_BAR; PG8_MMA(1, 0, At, B0); PG8_MMA(1, 1, At, B1); PG8_BAR; PG8_SCHED;
	ds_read_b128 v[0:3], v172
	ds_read_b128 v[4:7], v172 offset:1024
	ds_read_b128 v[8:11], v172 offset:2048
	ds_read_b128 v[12:15], v172 offset:3072
	ds_read_b128 v[16:19], v173
	ds_read_b128 v[20:23], v173 offset:1024
	ds_read_b128 v[24:27], v173 offset:2048
	ds_read_b128 v[28:31], v173 offset:3072
	ds_read_b128 v[174:177], v169 offset:32768
	ds_read_b128 v[178:181], v169 offset:33792
	ds_read_b128 v[182:185], v169 offset:34816
	ds_read_b128 v[186:189], v169 offset:35840
	ds_read_b128 v[190:193], v169 offset:36864
	ds_read_b128 v[194:197], v169 offset:37888
	ds_read_b128 v[198:201], v169 offset:38912
	ds_read_b128 v[202:205], v169 offset:39936
	s_mov_b32 m0, s65
	s_nop 0
	global_load_lds_dwordx4 v161, s[56:57]
	s_nop 0
	s_mov_b32 m0, s66
	s_nop 0
	global_load_lds_dwordx4 v165, s[56:57]
	s_waitcnt vmcnt(8)
	s_waitcnt lgkmcnt(0)
	s_barrier
	s_setprio 1
	s_waitcnt lgkmcnt(6)
	v_mfma_scale_f32_16x16x128_f8f6f4 v[156:159], v[0:7], v[174:181], v[156:159], v170, v171 op_sel_hi:[0,0,0]
	v_mfma_scale_f32_16x16x128_f8f6f4 v[152:155], v[8:15], v[174:181], v[152:155], v170, v171 op_sel_hi:[0,0,0]
	s_waitcnt lgkmcnt(4)
	v_mfma_scale_f32_16x16x128_f8f6f4 v[140:143], v[0:7], v[182:189], v[140:143], v170, v171 op_sel_hi:[0,0,0]
	v_mfma_scale_f32_16x16x128_f8f6f4 v[136:139], v[8:15], v[182:189], v[136:139], v170, v171 op_sel_hi:[0,0,0]
	s_waitcnt lgkmcnt(2)
	v_mfma_scale_f32_16x16x128_f8f6f4 v[124:127], v[0:7], v[190:197], v[124:127], v170, v171 op_sel_hi:[0,0,0]
	v_mfma_scale_f32_16x16x128_f8f6f4 v[120:123], v[8:15], v[190:197], v[120:123], v170, v171 op_sel_hi:[0,0,0]
	s_waitcnt lgkmcnt(0)
	v_mfma_scale_f32_16x16x128_f8f6f4 v[108:111], v[0:7], v[198:205], v[108:111], v170, v171 op_sel_hi:[0,0,0]
	v_mfma_scale_f32_16x16x128_f8f6f4 v[104:107], v[8:15], v[198:205], v[104:107], v170, v171 op_sel_hi:[0,0,0]
	s_setprio 0
	s_setprio 1
	v_mfma_scale_f32_16x16x128_f8f6f4 v[148:151], v[16:23], v[174:181], v[148:151], v170, v171 op_sel_hi:[0,0,0]
	v_mfma_scale_f32_16x16x128_f8f6f4 v[144:147], v[24:31], v[174:181], v[144:147], v170, v171 op_sel_hi:[0,0,0]
	v_mfma_scale_f32_16x16x128_f8f6f4 v[132:135], v[16:23], v[182:189], v[132:135], v170, v171 op_sel_hi:[0,0,0]
	v_mfma_scale_f32_16x16x128_f8f6f4 v[128:131], v[24:31], v[182:189], v[128:131], v170, v171 op_sel_hi:[0,0,0]
	v_mfma_scale_f32_16x16x128_f8f6f4 v[116:119], v[16:23], v[190:197], v[116:119], v170, v171 op_sel_hi:[0,0,0]
	v_mfma_scale_f32_16x16x128_f8f6f4 v[112:115], v[24:31], v[190:197], v[112:115], v170, v171 op_sel_hi:[0,0,0]
	v_mfma_scale_f32_16x16x128_f8f6f4 v[100:103], v[16:23], v[198:205], v[100:103], v170, v171 op_sel_hi:[0,0,0]
	v_mfma_scale_f32_16x16x128_f8f6f4 v[96:99], v[24:31], v[198:205], v[96:99], v170, v171 op_sel_hi:[0,0,0]
	s_setprio 0
	s_barrier
	ds_read_b128 v[174:177], v169 offset:49152
	ds_read_b128 v[178:181], v169 offset:50176
	ds_read_b128 v[182:185], v169 offset:51200
	ds_read_b128 v[186:189], v169 offset:52224
	ds_read_b128 v[190:193], v169 offset:53248
	ds_read_b128 v[194:197], v169 offset:54272
	ds_read_b128 v[198:201], v169 offset:55296
	ds_read_b128 v[202:205], v169 offset:56320
	s_add_u32 s22, s52, 0x80
	s_addc_u32 s23, s53, 0
	s_mov_b32 m0, s69
	s_nop 0
	global_load_lds_dwordx4 v162, s[22:23]
	s_nop 0
	s_mov_b32 m0, s70
	s_nop 0
	global_load_lds_dwordx4 v167, s[22:23]
	s_add_u32 s22, s52, 0x40080
	s_addc_u32 s23, s53, 0
	s_mov_b32 m0, s73
	s_nop 0
	global_load_lds_dwordx4 v162, s[22:23]
	s_nop 0
	s_mov_b32 m0, s74
	s_nop 0
	global_load_lds_dwordx4 v167, s[22:23]
	s_nop 0
	s_waitcnt vmcnt(6)
	s_waitcnt lgkmcnt(0)
	s_barrier
	s_setprio 1
	s_waitcnt lgkmcnt(6)
	v_mfma_scale_f32_16x16x128_f8f6f4 v[92:95], v[0:7], v[174:181], v[92:95], v170, v171 op_sel_hi:[0,0,0]
	v_mfma_scale_f32_16x16x128_f8f6f4 v[88:91], v[8:15], v[174:181], v[88:91], v170, v171 op_sel_hi:[0,0,0]
	s_mov_b32 m0, s71
	s_nop 0
	global_load_lds_dwordx4 v160, s[54:55]
	s_waitcnt lgkmcnt(4)
	v_mfma_scale_f32_16x16x128_f8f6f4 v[76:79], v[0:7], v[182:189], v[76:79], v170, v171 op_sel_hi:[0,0,0]
	v_mfma_scale_f32_16x16x128_f8f6f4 v[72:75], v[8:15], v[182:189], v[72:75], v170, v171 op_sel_hi:[0,0,0]
	s_mov_b32 m0, s72
	s_nop 0
	global_load_lds_dwordx4 v163, s[54:55]
	s_waitcnt lgkmcnt(2)
	v_mfma_scale_f32_16x16x128_f8f6f4 v[52:55], v[0:7], v[190:197], v[52:55], v170, v171 op_sel_hi:[0,0,0]
	v_mfma_scale_f32_16x16x128_f8f6f4 v[48:51], v[8:15], v[190:197], v[48:51], v170, v171 op_sel_hi:[0,0,0]
	s_waitcnt lgkmcnt(0)
	v_mfma_scale_f32_16x16x128_f8f6f4 v[36:39], v[0:7], v[198:205], v[36:39], v170, v171 op_sel_hi:[0,0,0]
	v_mfma_scale_f32_16x16x128_f8f6f4 v[32:35], v[8:15], v[198:205], v[32:35], v170, v171 op_sel_hi:[0,0,0]
	s_setprio 0
	s_setprio 1
	v_mfma_scale_f32_16x16x128_f8f6f4 v[84:87], v[16:23], v[174:181], v[84:87], v170, v171 op_sel_hi:[0,0,0]
	v_mfma_scale_f32_16x16x128_f8f6f4 v[80:83], v[24:31], v[174:181], v[80:83], v170, v171 op_sel_hi:[0,0,0]
	v_mfma_scale_f32_16x16x128_f8f6f4 v[68:71], v[16:23], v[182:189], v[68:71], v170, v171 op_sel_hi:[0,0,0]
	v_mfma_scale_f32_16x16x128_f8f6f4 v[56:59], v[24:31], v[182:189], v[56:59], v170, v171 op_sel_hi:[0,0,0]
	v_mfma_scale_f32_16x16x128_f8f6f4 v[64:67], v[16:23], v[190:197], v[64:67], v170, v171 op_sel_hi:[0,0,0]
	v_mfma_scale_f32_16x16x128_f8f6f4 v[60:63], v[24:31], v[190:197], v[60:63], v170, v171 op_sel_hi:[0,0,0]
	v_mfma_scale_f32_16x16x128_f8f6f4 v[44:47], v[16:23], v[198:205], v[44:47], v170, v171 op_sel_hi:[0,0,0]
	v_mfma_scale_f32_16x16x128_f8f6f4 v[40:43], v[24:31], v[198:205], v[40:43], v170, v171 op_sel_hi:[0,0,0]
	s_setprio 0
	s_barrier
	s_add_i32 s90, s90, 2
	s_add_u32 s88, s88, 0x100
	s_addc_u32 s89, s89, 0
	s_cmp_gt_u32 s90, 13
	s_mov_b64 s[50:51], s[48:49]
	s_cbranch_scc0 .LBB0_2753
	s_and_b64 vcc, exec, s[10:11]
	s_cbranch_vccz .LBB0_2756
	s_barrier
